# adds: P3 epilogue row-sum reductions with DPP row rotations instead of ds_bpermute round trips
# speedup vs baseline: 1.0212x; 1.0083x over previous
;     __device__ __forceinline__ void epilogue(f32x4 (&acc)[8][4], const Desc& d, unsigned char* stg) const {
;         const int tid = otid(), lane = tid & 63, wid = tid >> 6, l15 = lane & 15, gq = lane >> 4;
;         const int wr = wid >> 2, wc = wid & 3;
;         const int mt = d.mt, nt = d.nt, b = mt >> 5;
;         const int c = lane & 15, rsub = lane >> 4;
;         const int col = nt * 256 + wc * 64 + c * 4;
;         float4 g1 = *(const float4*)(p.mod + b * 6144 + 2048 + col);
;         g1.x *= 1.f / (O8S * W8S); g1.y *= 1.f / (O8S * W8S); g1.z *= 1.f / (O8S * W8S); g1.w *= 1.f / (O8S * W8S);
;         const size_t rowb = (size_t)mt * 256 + wr * 128 + rsub;
;         float4 xn[4]; float fn[4];
; #pragma unroll
;         for (int i2 = 0; i2 < 4; ++i2) { xn[i2] = *(const float4*)(p.x + (rowb + i2 * 4) * D + col); fn[i2] = p.rs[rowb + i2 * 4].y; }
; #pragma unroll
;         for (int m = 0; m < 8; ++m) {
;             float4 xc[4]; float fc[4];
; #pragma unroll
;             for (int i2 = 0; i2 < 4; ++i2) { xc[i2] = xn[i2]; fc[i2] = fn[i2]; }
;             if (m < 7) {
; #pragma unroll
;                 for (int i2 = 0; i2 < 4; ++i2) { xn[i2] = *(const float4*)(p.x + (rowb + (m + 1) * 16 + i2 * 4) * D + col); fn[i2] = p.rs[rowb + (m + 1) * 16 + i2 * 4].y; }
;             }
; #pragma unroll
;             for (int n = 0; n < 4; ++n) stgf_put(stg, n, acc[m][n], l15, gq);
;             asm volatile("s_waitcnt lgkmcnt(0)" ::: "memory");
; #pragma unroll
;             for (int i2 = 0; i2 < 4; ++i2) {
;                 const int rl = i2 * 4 + rsub;
;                 const size_t row = rowb + m * 16 + i2 * 4;
;                 const f32x4 v = stgf_get(stg, rl, c);
;                 const float fsm = fc[i2];
;                 const float4 xv = xc[i2];
;                 float4 r;
;                 r.x = xv.x + g1.x * (v[0] * fsm); r.y = xv.y + g1.y * (v[1] * fsm); r.z = xv.z + g1.z * (v[2] * fsm); r.w = xv.w + g1.w * (v[3] * fsm);
;                 *(uint2*)(p.x1 + row * D + col) = pack4((f32x4){r.x, r.y, r.z, r.w});
;                 float ss = r.x * r.x + r.y * r.y + r.z * r.z + r.w * r.w;
;                 ss += __shfl_xor(ss, 8); ss += __shfl_xor(ss, 4); ss += __shfl_xor(ss, 2); ss += __shfl_xor(ss, 1);
;                 if (c == 0) p.st2[row * 16 + nt * 4 + wc] = ss;
;             }
;             asm volatile("s_waitcnt lgkmcnt(0)" ::: "memory");
.LBB0_533:
	s_not_b32 s0, s29
	s_lshl_b32 s0, s0, 16
	s_and_b32 s0, s0, 0x10000
	v_mov_b32_e32 v183, v0
	s_waitcnt lgkmcnt(0)
	s_barrier
	s_add_i32 s5, s3, s0
	s_lshr_b32 s0, s22, 5
	v_and_b32_e32 v205, 15, v183
	v_bfe_u32 v221, v183, 6, 2
	s_lshl_b32 s1, s4, 8
	v_lshlrev_b32_e32 v2, 6, v221
	v_lshlrev_b32_e32 v116, 2, v205
	s_mulk_i32 s0, 0x1800
	v_or3_b32 v2, v2, s1, v116
	s_ashr_i32 s1, s0, 31
	s_lshl_b64 s[0:1], s[0:1], 2
	s_add_u32 s0, s78, s0
	s_addc_u32 s1, s79, s1
	v_lshlrev_b64 v[116:117], 2, v[2:3]
	v_lshl_add_u64 v[118:119], s[0:1], 0, v[116:117]
	v_add_co_u32_e32 v118, vcc, s28, v118
	s_lshl_b64 s[0:1], s[22:23], 8
	s_nop 0
	v_addc_co_u32_e32 v119, vcc, 0, v119, vcc
	global_load_dwordx4 v[178:181], v[118:119], off nt
	v_ashrrev_i32_e32 v118, 1, v183
	v_and_b32_e32 v118, 0xffffff80, v118
	v_ashrrev_i32_e32 v119, 31, v118
	v_bfe_u32 v222, v183, 4, 2
	v_lshl_add_u64 v[176:177], s[0:1], 0, v[118:119]
	v_or_b32_e32 v176, v176, v222
	v_or_b32_e32 v200, 12, v176
	v_mov_b32_e32 v201, v177
	v_lshl_add_u64 v[118:119], v[200:201], 3, s[10:11]
	global_load_dword v204, v[118:119], off offset:4
	v_lshl_add_u64 v[118:119], v[176:177], 3, s[10:11]
	v_or_b32_e32 v210, 4, v176
	v_mov_b32_e32 v211, v177
	v_lshl_add_u64 v[184:185], s[52:53], 0, v[116:117]
	global_load_dword v182, v[118:119], off offset:4
	v_lshlrev_b64 v[118:119], 12, v[210:211]
	v_lshl_add_u64 v[118:119], v[184:185], 0, v[118:119]
	global_load_dwordx4 v[156:159], v[118:119], off nt
	v_lshl_add_u64 v[118:119], v[210:211], 3, s[10:11]
	v_or_b32_e32 v206, 8, v176
	v_mov_b32_e32 v207, v177
	global_load_dword v212, v[118:119], off offset:4
	v_lshlrev_b64 v[118:119], 12, v[206:207]
	v_lshl_add_u64 v[118:119], v[184:185], 0, v[118:119]
	v_lshlrev_b64 v[116:117], 12, v[176:177]
	global_load_dwordx4 v[148:151], v[118:119], off nt
	v_lshl_add_u64 v[118:119], v[206:207], 3, s[10:11]
	v_lshl_add_u64 v[116:117], v[184:185], 0, v[116:117]
	global_load_dword v208, v[118:119], off offset:4
	global_load_dwordx4 v[224:227], v[116:117], off nt
	v_lshlrev_b64 v[116:117], 12, v[200:201]
	v_lshl_add_u64 v[116:117], v[184:185], 0, v[116:117]
	v_or_b32_e32 v198, 16, v176
	v_mov_b32_e32 v199, v177
	global_load_dwordx4 v[152:155], v[116:117], off nt
	v_lshlrev_b64 v[116:117], 12, v[198:199]
	v_lshl_add_u64 v[116:117], v[184:185], 0, v[116:117]
	v_or_b32_e32 v186, 28, v176
	v_mov_b32_e32 v187, v177
	global_load_dwordx4 v[144:147], v[116:117], off nt
	v_lshl_add_u64 v[116:117], v[198:199], 3, s[10:11]
	v_or_b32_e32 v194, 20, v176
	v_mov_b32_e32 v195, v177
	v_lshl_add_u64 v[216:217], v[186:187], 3, s[10:11]
	global_load_dword v202, v[116:117], off offset:4
	global_load_dword v188, v[216:217], off offset:4
	v_lshlrev_b64 v[116:117], 12, v[194:195]
	v_lshl_add_u64 v[116:117], v[184:185], 0, v[116:117]
	global_load_dwordx4 v[140:143], v[116:117], off nt
	v_lshl_add_u64 v[116:117], v[194:195], 3, s[10:11]
	v_or_b32_e32 v190, 24, v176
	v_mov_b32_e32 v191, v177
	global_load_dword v196, v[116:117], off offset:4
	v_lshlrev_b64 v[116:117], 12, v[190:191]
	v_lshl_add_u64 v[116:117], v[184:185], 0, v[116:117]
	global_load_dwordx4 v[136:139], v[116:117], off nt
	v_lshl_add_u64 v[116:117], v[190:191], 3, s[10:11]
	global_load_dword v192, v[116:117], off offset:4
	v_lshlrev_b64 v[116:117], 12, v[186:187]
	v_lshl_add_u64 v[116:117], v[184:185], 0, v[116:117]
	global_load_dwordx4 v[116:119], v[116:117], off nt
	v_lshrrev_b32_e32 v183, 4, v183
	v_bitop3_b32 v183, v183, v205, 3 bitop3:0x6c
	v_lshl_add_u32 v209, v205, 8, s5
	v_lshlrev_b32_e32 v183, 4, v183
	v_add_u32_e32 v216, v209, v183
	ds_write_b128 v216, v[132:135]
	v_bitop3_b32 v132, v222, v205, 4 bitop3:0x36
	v_lshlrev_b32_e32 v132, 4, v132
	v_add_u32_e32 v217, v209, v132
	ds_write_b128 v217, v[128:131]
	v_bitop3_b32 v128, v222, v205, 8 bitop3:0x36
	v_lshlrev_b32_e32 v128, 4, v128
	v_add_u32_e32 v218, v209, v128
	ds_write_b128 v218, v[124:127]
	v_bitop3_b32 v124, v222, v205, 12 bitop3:0x36
	v_lshlrev_b32_e32 v124, 4, v124
	v_add_u32_e32 v219, v209, v124
	ds_write_b128 v219, v[120:123]
	v_lshl_add_u32 v120, v222, 8, s5
	v_and_b32_e32 v121, 64, v214
	v_add_u32_e32 v220, v120, v183
	v_xor_b32_e32 v120, 8, v214
	v_add_u32_e32 v125, 64, v121
	v_cmp_lt_i32_e64 s[0:1], v120, v125
	s_waitcnt lgkmcnt(0)
	v_cmp_eq_u32_e32 vcc, 0, v205
	v_xor_b32_e32 v126, 4, v214
	v_cndmask_b32_e64 v120, v214, v120, s[0:1]
	v_lshlrev_b32_e32 v205, 2, v120
	ds_read_b128 v[120:123], v220
	s_waitcnt vmcnt(0)
	v_pk_mul_f32 v[178:179], v[178:179], s[14:15] op_sel_hi:[1,0]
	v_cmp_lt_i32_e64 s[0:1], v126, v125
	v_pk_mul_f32 v[180:181], v[180:181], s[14:15] op_sel_hi:[1,0]
	v_xor_b32_e32 v129, 2, v214
	s_waitcnt lgkmcnt(0)
	v_pk_mul_f32 v[120:121], v[182:183], v[120:121] op_sel_hi:[0,1]
	v_cndmask_b32_e64 v126, v214, v126, s[0:1]
	v_pk_mul_f32 v[122:123], v[182:183], v[122:123] op_sel_hi:[0,1]
	v_lshlrev_b32_e32 v209, 2, v126
	v_cmp_lt_i32_e64 s[0:1], v129, v125
	s_lshl_b32 s22, s4, 2
	s_mov_b32 s23, s9
	v_cndmask_b32_e64 v129, v214, v129, s[0:1]
	v_lshlrev_b32_e32 v213, 2, v129
	v_xor_b32_e32 v129, 1, v214
	v_cmp_lt_i32_e64 s[0:1], v129, v125
	v_lshlrev_b32_e32 v182, 2, v221
	v_pk_fma_f32 v[120:121], v[178:179], v[120:121], v[224:225]
	v_pk_fma_f32 v[122:123], v[180:181], v[122:123], v[226:227]
	v_pk_mul_f32 v[126:127], v[120:121], v[120:121]
	v_pk_mul_f32 v[130:131], v[122:123], v[122:123]
	v_add_f32_e32 v126, v126, v127
	v_add_f32_e32 v126, v130, v126
	v_add_f32_e32 v126, v131, v126
	s_nop 1
	v_mov_b32_dpp v127, v126 row_ror:8 row_mask:0xf bank_mask:0xf
	v_cndmask_b32_e64 v125, v214, v129, s[0:1]
	v_lshlrev_b32_e32 v215, 2, v125
	v_mov_b32_e32 v131, v3
	s_waitcnt lgkmcnt(0)
	v_add_f32_e32 v127, v126, v127
	s_nop 1
	v_mov_b32_dpp v130, v127 row_ror:4 row_mask:0xf bank_mask:0xf
	v_cvt_pk_bf16_f32 v126, v120, v121
	v_lshlrev_b64 v[120:121], 11, v[176:177]
	s_waitcnt lgkmcnt(0)
	v_add_f32_e32 v125, v127, v130
	s_nop 1
	v_mov_b32_dpp v129, v125 quad_perm:[2,3,0,1] row_mask:0xf bank_mask:0xf
	v_cvt_pk_bf16_f32 v127, v122, v123
	v_lshl_add_u64 v[122:123], s[24:25], 0, v[120:121]
	v_lshlrev_b32_e32 v130, 1, v2
	v_lshl_add_u64 v[122:123], v[122:123], 0, v[130:131]
	s_waitcnt lgkmcnt(0)
	v_add_f32_e32 v120, v125, v129
	s_nop 1
	v_mov_b32_dpp v121, v120 quad_perm:[1,0,3,2] row_mask:0xf bank_mask:0xf
	global_store_dwordx2 v[122:123], v[126:127], off
	s_and_saveexec_b64 s[0:1], vcc
	s_cbranch_execz .LBB0_535
	v_lshlrev_b64 v[122:123], 6, v[176:177]
	v_lshl_add_u64 v[122:123], s[6:7], 0, v[122:123]
	v_lshl_add_u64 v[122:123], s[22:23], 2, v[122:123]
	v_mov_b32_e32 v183, v3
	v_lshl_add_u64 v[122:123], v[122:123], 0, v[182:183]
	s_waitcnt lgkmcnt(0)
	v_add_f32_e32 v120, v120, v121
	global_store_dword v[122:123], v120, off
; __device__ __forceinline__ uint2 pack4(f32x4 v) { uint2 r; r.x = pack2(v[0], v[1]); r.y = pack2(v[2], v[3]); return r; }
;     __device__ __forceinline__ void epilogue(f32x4 (&acc)[8][4], const Desc& d, unsigned char* stg) const {
;     ...
; #pragma unroll
;                 for (int i2 = 0; i2 < 4; ++i2) { xn[i2] = *(const float4*)(p.x + (rowb + (m + 1) * 16 + i2 * 4) * D + col); fn[i2] = p.rs[rowb + (m + 1) * 16 + i2 * 4].y; }
;             }
; #pragma unroll
;             for (int n = 0; n < 4; ++n) stgf_put(stg, n, acc[m][n], l15, gq);
;             asm volatile("s_waitcnt lgkmcnt(0)" ::: "memory");
; #pragma unroll
;             for (int i2 = 0; i2 < 4; ++i2) {
;                 const int rl = i2 * 4 + rsub;
;                 const size_t row = rowb + m * 16 + i2 * 4;
;                 const f32x4 v = stgf_get(stg, rl, c);
;                 const float fsm = fc[i2];
;                 const float4 xv = xc[i2];
;                 float4 r;
;                 r.x = xv.x + g1.x * (v[0] * fsm); r.y = xv.y + g1.y * (v[1] * fsm); r.z = xv.z + g1.z * (v[2] * fsm); r.w = xv.w + g1.w * (v[3] * fsm);
;                 *(uint2*)(p.x1 + row * D + col) = pack4((f32x4){r.x, r.y, r.z, r.w});
;                 float ss = r.x * r.x + r.y * r.y + r.z * r.z + r.w * r.w;
;                 ss += __shfl_xor(ss, 8); ss += __shfl_xor(ss, 4); ss += __shfl_xor(ss, 2); ss += __shfl_xor(ss, 1);
;                 if (c == 0) p.st2[row * 16 + nt * 4 + wc] = ss;
;             }
;             asm volatile("s_waitcnt lgkmcnt(0)" ::: "memory");
.LBB0_535:
	s_or_b64 exec, exec, s[0:1]
	v_or_b32_e32 v120, 4, v222
	v_lshl_add_u32 v120, v120, 8, s5
	v_add_u32_e32 v221, v120, v132
	s_waitcnt lgkmcnt(0)
	ds_read_b128 v[120:123], v221
	v_lshlrev_b32_e32 v2, 1, v2
	s_waitcnt lgkmcnt(0)
	v_pk_mul_f32 v[120:121], v[212:213], v[120:121] op_sel_hi:[0,1]
	v_pk_mul_f32 v[122:123], v[212:213], v[122:123] op_sel_hi:[0,1]
	v_pk_fma_f32 v[120:121], v[178:179], v[120:121], v[156:157]
	v_pk_fma_f32 v[122:123], v[180:181], v[122:123], v[158:159]
	v_pk_mul_f32 v[126:127], v[120:121], v[120:121]
	v_pk_mul_f32 v[130:131], v[122:123], v[122:123]
	v_add_f32_e32 v125, v126, v127
	v_add_f32_e32 v125, v130, v125
	v_add_f32_e32 v125, v131, v125
	s_nop 1
	v_mov_b32_dpp v126, v125 row_ror:8 row_mask:0xf bank_mask:0xf
	v_cvt_pk_bf16_f32 v127, v122, v123
	v_lshlrev_b64 v[122:123], 11, v[210:211]
	v_lshl_add_u64 v[122:123], s[24:25], 0, v[122:123]
	v_lshl_add_u64 v[122:123], v[122:123], 0, v[2:3]
	s_waitcnt lgkmcnt(0)
	v_add_f32_e32 v125, v125, v126
	s_nop 1
	v_mov_b32_dpp v126, v125 row_ror:4 row_mask:0xf bank_mask:0xf
	s_waitcnt lgkmcnt(0)
	v_add_f32_e32 v125, v125, v126
	s_nop 1
	v_mov_b32_dpp v129, v125 quad_perm:[2,3,0,1] row_mask:0xf bank_mask:0xf
	v_cvt_pk_bf16_f32 v126, v120, v121
	global_store_dwordx2 v[122:123], v[126:127], off
	s_waitcnt lgkmcnt(0)
	v_add_f32_e32 v120, v125, v129
	s_nop 1
	v_mov_b32_dpp v121, v120 quad_perm:[1,0,3,2] row_mask:0xf bank_mask:0xf
	s_and_saveexec_b64 s[0:1], vcc
	s_cbranch_execz .LBB0_537
	v_lshlrev_b64 v[122:123], 6, v[210:211]
	v_lshl_add_u64 v[122:123], s[6:7], 0, v[122:123]
	v_lshl_add_u64 v[122:123], s[22:23], 2, v[122:123]
	v_mov_b32_e32 v183, v3
	v_lshl_add_u64 v[122:123], v[122:123], 0, v[182:183]
	s_waitcnt lgkmcnt(0)
	v_add_f32_e32 v120, v120, v121
	global_store_dword v[122:123], v120, off
.LBB0_537:
	s_or_b64 exec, exec, s[0:1]
	v_or_b32_e32 v120, 8, v222
	v_lshl_add_u32 v120, v120, 8, s5
	v_add_u32_e32 v159, v120, v128
	s_waitcnt lgkmcnt(0)
	ds_read_b128 v[120:123], v159
	s_waitcnt lgkmcnt(0)
	v_pk_mul_f32 v[120:121], v[208:209], v[120:121] op_sel_hi:[0,1]
	v_pk_mul_f32 v[122:123], v[208:209], v[122:123] op_sel_hi:[0,1]
	v_pk_fma_f32 v[120:121], v[178:179], v[120:121], v[148:149]
	v_pk_fma_f32 v[122:123], v[180:181], v[122:123], v[150:151]
	v_pk_mul_f32 v[126:127], v[120:121], v[120:121]
	v_pk_mul_f32 v[128:129], v[122:123], v[122:123]
	v_add_f32_e32 v125, v126, v127
	v_add_f32_e32 v125, v128, v125
	v_add_f32_e32 v125, v129, v125
	s_nop 1
	v_mov_b32_dpp v126, v125 row_ror:8 row_mask:0xf bank_mask:0xf
	v_cvt_pk_bf16_f32 v127, v122, v123
	v_lshlrev_b64 v[122:123], 11, v[206:207]
	v_lshl_add_u64 v[122:123], s[24:25], 0, v[122:123]
	v_lshl_add_u64 v[122:123], v[122:123], 0, v[2:3]
	s_waitcnt lgkmcnt(0)
	v_add_f32_e32 v125, v125, v126
	s_nop 1
	v_mov_b32_dpp v126, v125 row_ror:4 row_mask:0xf bank_mask:0xf
	s_waitcnt lgkmcnt(0)
	v_add_f32_e32 v125, v125, v126
	s_nop 1
	v_mov_b32_dpp v128, v125 quad_perm:[2,3,0,1] row_mask:0xf bank_mask:0xf
	v_cvt_pk_bf16_f32 v126, v120, v121
	global_store_dwordx2 v[122:123], v[126:127], off
	s_waitcnt lgkmcnt(0)
	v_add_f32_e32 v120, v125, v128
	s_nop 1
	v_mov_b32_dpp v121, v120 quad_perm:[1,0,3,2] row_mask:0xf bank_mask:0xf
	s_and_saveexec_b64 s[0:1], vcc
	s_cbranch_execz .LBB0_539
	v_lshlrev_b64 v[122:123], 6, v[206:207]
	v_lshl_add_u64 v[122:123], s[6:7], 0, v[122:123]
	v_lshl_add_u64 v[122:123], s[22:23], 2, v[122:123]
	v_mov_b32_e32 v183, v3
	v_lshl_add_u64 v[122:123], v[122:123], 0, v[182:183]
	s_waitcnt lgkmcnt(0)
	v_add_f32_e32 v120, v120, v121
	global_store_dword v[122:123], v120, off
.LBB0_539:
	s_or_b64 exec, exec, s[0:1]
	v_or_b32_e32 v120, 12, v222
	v_lshl_add_u32 v120, v120, 8, s5
	v_add_u32_e32 v151, v120, v124
	s_waitcnt lgkmcnt(0)
	ds_read_b128 v[120:123], v151
	s_waitcnt lgkmcnt(0)
	v_pk_mul_f32 v[120:121], v[204:205], v[120:121] op_sel_hi:[0,1]
	v_pk_mul_f32 v[122:123], v[204:205], v[122:123] op_sel_hi:[0,1]
	v_pk_fma_f32 v[120:121], v[178:179], v[120:121], v[152:153]
	v_pk_fma_f32 v[122:123], v[180:181], v[122:123], v[154:155]
	v_pk_mul_f32 v[124:125], v[120:121], v[120:121]
	v_pk_mul_f32 v[126:127], v[122:123], v[122:123]
	v_add_f32_e32 v124, v124, v125
	v_add_f32_e32 v124, v126, v124
	v_add_f32_e32 v124, v127, v124
	s_nop 1
	v_mov_b32_dpp v125, v124 row_ror:8 row_mask:0xf bank_mask:0xf
	s_waitcnt lgkmcnt(0)
	v_add_f32_e32 v124, v124, v125
	s_nop 1
	v_mov_b32_dpp v125, v124 row_ror:4 row_mask:0xf bank_mask:0xf
	s_waitcnt lgkmcnt(0)
	v_add_f32_e32 v126, v124, v125
	s_nop 1
	v_mov_b32_dpp v127, v126 quad_perm:[2,3,0,1] row_mask:0xf bank_mask:0xf
	v_cvt_pk_bf16_f32 v124, v120, v121
	v_cvt_pk_bf16_f32 v125, v122, v123
	v_lshlrev_b64 v[122:123], 11, v[200:201]
	v_lshl_add_u64 v[122:123], s[24:25], 0, v[122:123]
	s_waitcnt lgkmcnt(0)
	v_add_f32_e32 v120, v126, v127
	s_nop 1
	v_mov_b32_dpp v121, v120 quad_perm:[1,0,3,2] row_mask:0xf bank_mask:0xf
	v_lshl_add_u64 v[122:123], v[122:123], 0, v[2:3]
	global_store_dwordx2 v[122:123], v[124:125], off
	s_and_saveexec_b64 s[0:1], vcc
	s_cbranch_execz .LBB0_541
	v_lshlrev_b64 v[122:123], 6, v[200:201]
	v_lshl_add_u64 v[122:123], s[6:7], 0, v[122:123]
	v_lshl_add_u64 v[122:123], s[22:23], 2, v[122:123]
	v_mov_b32_e32 v183, v3
	v_lshl_add_u64 v[122:123], v[122:123], 0, v[182:183]
	s_waitcnt lgkmcnt(0)
	v_add_f32_e32 v120, v120, v121
	global_store_dword v[122:123], v120, off
; __device__ __forceinline__ uint2 pack4(f32x4 v) { uint2 r; r.x = pack2(v[0], v[1]); r.y = pack2(v[2], v[3]); return r; }
;     __device__ __forceinline__ void epilogue(f32x4 (&acc)[8][4], const Desc& d, unsigned char* stg) const {
;     ...
;         for (int m = 0; m < 8; ++m) {
;             float4 xc[4]; float fc[4];
; #pragma unroll
;             for (int i2 = 0; i2 < 4; ++i2) { xc[i2] = xn[i2]; fc[i2] = fn[i2]; }
;             if (m < 7) {
; #pragma unroll
;                 for (int i2 = 0; i2 < 4; ++i2) { xn[i2] = *(const float4*)(p.x + (rowb + (m + 1) * 16 + i2 * 4) * D + col); fn[i2] = p.rs[rowb + (m + 1) * 16 + i2 * 4].y; }
;             }
; #pragma unroll
;             for (int n = 0; n < 4; ++n) stgf_put(stg, n, acc[m][n], l15, gq);
;             asm volatile("s_waitcnt lgkmcnt(0)" ::: "memory");
; #pragma unroll
;             for (int i2 = 0; i2 < 4; ++i2) {
;                 const int rl = i2 * 4 + rsub;
;                 const size_t row = rowb + m * 16 + i2 * 4;
;                 const f32x4 v = stgf_get(stg, rl, c);
;                 const float fsm = fc[i2];
;                 const float4 xv = xc[i2];
;                 float4 r;
;                 r.x = xv.x + g1.x * (v[0] * fsm); r.y = xv.y + g1.y * (v[1] * fsm); r.z = xv.z + g1.z * (v[2] * fsm); r.w = xv.w + g1.w * (v[3] * fsm);
;                 *(uint2*)(p.x1 + row * D + col) = pack4((f32x4){r.x, r.y, r.z, r.w});
;                 float ss = r.x * r.x + r.y * r.y + r.z * r.z + r.w * r.w;
;                 ss += __shfl_xor(ss, 8); ss += __shfl_xor(ss, 4); ss += __shfl_xor(ss, 2); ss += __shfl_xor(ss, 1);
;                 if (c == 0) p.st2[row * 16 + nt * 4 + wc] = ss;
;             }
;             asm volatile("s_waitcnt lgkmcnt(0)" ::: "memory");
.LBB0_541:
	s_or_b64 exec, exec, s[0:1]
	v_or_b32_e32 v200, 32, v176
	v_mov_b32_e32 v201, v177
	s_waitcnt lgkmcnt(0)
	v_lshlrev_b64 v[120:121], 12, v[200:201]
	s_waitcnt lgkmcnt(0)
	v_lshl_add_u64 v[120:121], v[184:185], 0, v[120:121]
	v_or_b32_e32 v148, 44, v176
	v_mov_b32_e32 v149, v177
	global_load_dwordx4 v[132:135], v[120:121], off nt
	v_lshl_add_u64 v[120:121], v[200:201], 3, s[10:11]
	v_or_b32_e32 v156, 36, v176
	v_mov_b32_e32 v157, v177
	v_lshl_add_u64 v[206:207], v[148:149], 3, s[10:11]
	global_load_dword v204, v[120:121], off offset:4
	global_load_dword v150, v[206:207], off offset:4
	v_lshlrev_b64 v[120:121], 12, v[156:157]
	v_lshl_add_u64 v[120:121], v[184:185], 0, v[120:121]
	global_load_dwordx4 v[128:131], v[120:121], off nt
	v_lshl_add_u64 v[120:121], v[156:157], 3, s[10:11]
	v_or_b32_e32 v152, 40, v176
	v_mov_b32_e32 v153, v177
	global_load_dword v158, v[120:121], off offset:4
	v_lshlrev_b64 v[120:121], 12, v[152:153]
	v_lshl_add_u64 v[120:121], v[184:185], 0, v[120:121]
	global_load_dwordx4 v[124:127], v[120:121], off nt
	v_lshl_add_u64 v[120:121], v[152:153], 3, s[10:11]
	global_load_dword v154, v[120:121], off offset:4
	v_lshlrev_b64 v[120:121], 12, v[148:149]
	v_lshl_add_u64 v[120:121], v[184:185], 0, v[120:121]
	global_load_dwordx4 v[120:123], v[120:121], off nt
	ds_write_b128 v216, v[100:103]
	ds_write_b128 v217, v[104:107]
	ds_write_b128 v218, v[108:111]
	ds_write_b128 v219, v[112:115]
	s_waitcnt lgkmcnt(0)
	ds_read_b128 v[100:103], v220
	s_waitcnt lgkmcnt(0)
	v_pk_mul_f32 v[100:101], v[202:203], v[100:101] op_sel_hi:[0,1]
	v_pk_fma_f32 v[100:101], v[178:179], v[100:101], v[144:145]
	v_pk_mul_f32 v[102:103], v[202:203], v[102:103] op_sel_hi:[0,1]
	v_pk_fma_f32 v[102:103], v[180:181], v[102:103], v[146:147]
	v_pk_mul_f32 v[104:105], v[100:101], v[100:101]
	v_pk_mul_f32 v[106:107], v[102:103], v[102:103]
	v_add_f32_e32 v104, v104, v105
	v_add_f32_e32 v104, v106, v104
	v_add_f32_e32 v104, v107, v104
	s_nop 1
	v_mov_b32_dpp v105, v104 row_ror:8 row_mask:0xf bank_mask:0xf
	s_waitcnt lgkmcnt(0)
	v_add_f32_e32 v104, v104, v105
	s_nop 1
	v_mov_b32_dpp v105, v104 row_ror:4 row_mask:0xf bank_mask:0xf
	s_waitcnt lgkmcnt(0)
	v_add_f32_e32 v106, v104, v105
	s_nop 1
	v_mov_b32_dpp v107, v106 quad_perm:[2,3,0,1] row_mask:0xf bank_mask:0xf
	v_cvt_pk_bf16_f32 v104, v100, v101
	v_cvt_pk_bf16_f32 v105, v102, v103
	v_lshlrev_b64 v[102:103], 11, v[198:199]
	v_lshl_add_u64 v[102:103], s[24:25], 0, v[102:103]
	s_waitcnt lgkmcnt(0)
	v_add_f32_e32 v100, v106, v107
	s_nop 1
	v_mov_b32_dpp v101, v100 quad_perm:[1,0,3,2] row_mask:0xf bank_mask:0xf
	v_lshl_add_u64 v[102:103], v[102:103], 0, v[2:3]
	global_store_dwordx2 v[102:103], v[104:105], off
	s_and_saveexec_b64 s[0:1], vcc
	s_cbranch_execz .LBB0_543
	v_lshlrev_b64 v[102:103], 6, v[198:199]
	v_lshl_add_u64 v[102:103], s[6:7], 0, v[102:103]
	v_lshl_add_u64 v[102:103], s[22:23], 2, v[102:103]
	v_mov_b32_e32 v183, v3
	v_lshl_add_u64 v[102:103], v[102:103], 0, v[182:183]
	s_waitcnt lgkmcnt(0)
	v_add_f32_e32 v100, v100, v101
	global_store_dword v[102:103], v100, off
.LBB0_543:
	s_or_b64 exec, exec, s[0:1]
	s_waitcnt lgkmcnt(0)
	ds_read_b128 v[100:103], v221
	s_waitcnt lgkmcnt(0)
	v_pk_mul_f32 v[100:101], v[196:197], v[100:101] op_sel_hi:[0,1]
	v_pk_mul_f32 v[102:103], v[196:197], v[102:103] op_sel_hi:[0,1]
	v_pk_fma_f32 v[100:101], v[178:179], v[100:101], v[140:141]
	v_pk_fma_f32 v[102:103], v[180:181], v[102:103], v[142:143]
	v_pk_mul_f32 v[104:105], v[100:101], v[100:101]
	v_pk_mul_f32 v[106:107], v[102:103], v[102:103]
	v_add_f32_e32 v104, v104, v105
	v_add_f32_e32 v104, v106, v104
	v_add_f32_e32 v104, v107, v104
	s_nop 1
	v_mov_b32_dpp v105, v104 row_ror:8 row_mask:0xf bank_mask:0xf
	s_waitcnt lgkmcnt(0)
	v_add_f32_e32 v104, v104, v105
	s_nop 1
	v_mov_b32_dpp v105, v104 row_ror:4 row_mask:0xf bank_mask:0xf
	s_waitcnt lgkmcnt(0)
	v_add_f32_e32 v106, v104, v105
	s_nop 1
	v_mov_b32_dpp v107, v106 quad_perm:[2,3,0,1] row_mask:0xf bank_mask:0xf
	v_cvt_pk_bf16_f32 v104, v100, v101
	v_cvt_pk_bf16_f32 v105, v102, v103
	v_lshlrev_b64 v[102:103], 11, v[194:195]
	v_lshl_add_u64 v[102:103], s[24:25], 0, v[102:103]
	s_waitcnt lgkmcnt(0)
	v_add_f32_e32 v100, v106, v107
	s_nop 1
	v_mov_b32_dpp v101, v100 quad_perm:[1,0,3,2] row_mask:0xf bank_mask:0xf
	v_lshl_add_u64 v[102:103], v[102:103], 0, v[2:3]
	global_store_dwordx2 v[102:103], v[104:105], off
	s_and_saveexec_b64 s[0:1], vcc
	s_cbranch_execz .LBB0_545
	v_lshlrev_b64 v[102:103], 6, v[194:195]
	v_lshl_add_u64 v[102:103], s[6:7], 0, v[102:103]
	v_lshl_add_u64 v[102:103], s[22:23], 2, v[102:103]
	v_mov_b32_e32 v183, v3
	v_lshl_add_u64 v[102:103], v[102:103], 0, v[182:183]
	s_waitcnt lgkmcnt(0)
	v_add_f32_e32 v100, v100, v101
	global_store_dword v[102:103], v100, off
.LBB0_545:
	s_or_b64 exec, exec, s[0:1]
	s_waitcnt lgkmcnt(0)
	ds_read_b128 v[100:103], v159
	s_waitcnt lgkmcnt(0)
	v_pk_mul_f32 v[100:101], v[192:193], v[100:101] op_sel_hi:[0,1]
	v_pk_mul_f32 v[102:103], v[192:193], v[102:103] op_sel_hi:[0,1]
	v_pk_fma_f32 v[100:101], v[178:179], v[100:101], v[136:137]
	v_pk_fma_f32 v[102:103], v[180:181], v[102:103], v[138:139]
	v_pk_mul_f32 v[104:105], v[100:101], v[100:101]
	v_pk_mul_f32 v[106:107], v[102:103], v[102:103]
	v_add_f32_e32 v104, v104, v105
	v_add_f32_e32 v104, v106, v104
	v_add_f32_e32 v104, v107, v104
	s_nop 1
	v_mov_b32_dpp v105, v104 row_ror:8 row_mask:0xf bank_mask:0xf
	s_waitcnt lgkmcnt(0)
	v_add_f32_e32 v104, v104, v105
	s_nop 1
	v_mov_b32_dpp v105, v104 row_ror:4 row_mask:0xf bank_mask:0xf
	s_waitcnt lgkmcnt(0)
	v_add_f32_e32 v106, v104, v105
	s_nop 1
	v_mov_b32_dpp v107, v106 quad_perm:[2,3,0,1] row_mask:0xf bank_mask:0xf
	v_cvt_pk_bf16_f32 v104, v100, v101
	v_cvt_pk_bf16_f32 v105, v102, v103
	v_lshlrev_b64 v[102:103], 11, v[190:191]
	v_lshl_add_u64 v[102:103], s[24:25], 0, v[102:103]
	s_waitcnt lgkmcnt(0)
	v_add_f32_e32 v100, v106, v107
	s_nop 1
	v_mov_b32_dpp v101, v100 quad_perm:[1,0,3,2] row_mask:0xf bank_mask:0xf
	v_lshl_add_u64 v[102:103], v[102:103], 0, v[2:3]
	global_store_dwordx2 v[102:103], v[104:105], off
	s_and_saveexec_b64 s[0:1], vcc
	s_cbranch_execz .LBB0_547
	v_lshlrev_b64 v[102:103], 6, v[190:191]
	v_lshl_add_u64 v[102:103], s[6:7], 0, v[102:103]
	v_lshl_add_u64 v[102:103], s[22:23], 2, v[102:103]
	v_mov_b32_e32 v183, v3
	v_lshl_add_u64 v[102:103], v[102:103], 0, v[182:183]
	s_waitcnt lgkmcnt(0)
	v_add_f32_e32 v100, v100, v101
	global_store_dword v[102:103], v100, off
; __device__ __forceinline__ uint2 pack4(f32x4 v) { uint2 r; r.x = pack2(v[0], v[1]); r.y = pack2(v[2], v[3]); return r; }
;     __device__ __forceinline__ void epilogue(f32x4 (&acc)[8][4], const Desc& d, unsigned char* stg) const {
;     ...
;         for (int m = 0; m < 8; ++m) {
;             float4 xc[4]; float fc[4];
; #pragma unroll
;             for (int i2 = 0; i2 < 4; ++i2) { xc[i2] = xn[i2]; fc[i2] = fn[i2]; }
;             if (m < 7) {
; #pragma unroll
;                 for (int i2 = 0; i2 < 4; ++i2) { xn[i2] = *(const float4*)(p.x + (rowb + (m + 1) * 16 + i2 * 4) * D + col); fn[i2] = p.rs[rowb + (m + 1) * 16 + i2 * 4].y; }
;             }
; #pragma unroll
;             for (int n = 0; n < 4; ++n) stgf_put(stg, n, acc[m][n], l15, gq);
;             asm volatile("s_waitcnt lgkmcnt(0)" ::: "memory");
; #pragma unroll
;             for (int i2 = 0; i2 < 4; ++i2) {
;                 const int rl = i2 * 4 + rsub;
;                 const size_t row = rowb + m * 16 + i2 * 4;
;                 const f32x4 v = stgf_get(stg, rl, c);
;                 const float fsm = fc[i2];
;                 const float4 xv = xc[i2];
;                 float4 r;
;                 r.x = xv.x + g1.x * (v[0] * fsm); r.y = xv.y + g1.y * (v[1] * fsm); r.z = xv.z + g1.z * (v[2] * fsm); r.w = xv.w + g1.w * (v[3] * fsm);
;                 *(uint2*)(p.x1 + row * D + col) = pack4((f32x4){r.x, r.y, r.z, r.w});
;                 float ss = r.x * r.x + r.y * r.y + r.z * r.z + r.w * r.w;
;                 ss += __shfl_xor(ss, 8); ss += __shfl_xor(ss, 4); ss += __shfl_xor(ss, 2); ss += __shfl_xor(ss, 1);
;                 if (c == 0) p.st2[row * 16 + nt * 4 + wc] = ss;
;             }
;             asm volatile("s_waitcnt lgkmcnt(0)" ::: "memory");
.LBB0_547:
	s_or_b64 exec, exec, s[0:1]
	s_waitcnt lgkmcnt(0)
	ds_read_b128 v[100:103], v151
	s_waitcnt lgkmcnt(0)
	v_pk_mul_f32 v[100:101], v[188:189], v[100:101] op_sel_hi:[0,1]
	v_pk_mul_f32 v[102:103], v[188:189], v[102:103] op_sel_hi:[0,1]
	v_pk_fma_f32 v[100:101], v[178:179], v[100:101], v[116:117]
	v_pk_fma_f32 v[102:103], v[180:181], v[102:103], v[118:119]
	v_pk_mul_f32 v[104:105], v[100:101], v[100:101]
	v_pk_mul_f32 v[106:107], v[102:103], v[102:103]
	v_add_f32_e32 v104, v104, v105
	v_add_f32_e32 v104, v106, v104
	v_add_f32_e32 v104, v107, v104
	s_nop 1
	v_mov_b32_dpp v105, v104 row_ror:8 row_mask:0xf bank_mask:0xf
	s_waitcnt lgkmcnt(0)
	v_add_f32_e32 v104, v104, v105
	s_nop 1
	v_mov_b32_dpp v105, v104 row_ror:4 row_mask:0xf bank_mask:0xf
	s_waitcnt lgkmcnt(0)
	v_add_f32_e32 v106, v104, v105
	s_nop 1
	v_mov_b32_dpp v107, v106 quad_perm:[2,3,0,1] row_mask:0xf bank_mask:0xf
	v_cvt_pk_bf16_f32 v104, v100, v101
	v_cvt_pk_bf16_f32 v105, v102, v103
	v_lshlrev_b64 v[102:103], 11, v[186:187]
	v_lshl_add_u64 v[102:103], s[24:25], 0, v[102:103]
	s_waitcnt lgkmcnt(0)
	v_add_f32_e32 v100, v106, v107
	s_nop 1
	v_mov_b32_dpp v101, v100 quad_perm:[1,0,3,2] row_mask:0xf bank_mask:0xf
	v_lshl_add_u64 v[102:103], v[102:103], 0, v[2:3]
	global_store_dwordx2 v[102:103], v[104:105], off
	s_and_saveexec_b64 s[0:1], vcc
	s_cbranch_execz .LBB0_549
	v_lshlrev_b64 v[102:103], 6, v[186:187]
	v_lshl_add_u64 v[102:103], s[6:7], 0, v[102:103]
	v_lshl_add_u64 v[102:103], s[22:23], 2, v[102:103]
	v_mov_b32_e32 v183, v3
	v_lshl_add_u64 v[102:103], v[102:103], 0, v[182:183]
	s_waitcnt lgkmcnt(0)
	v_add_f32_e32 v100, v100, v101
	global_store_dword v[102:103], v100, off
.LBB0_549:
	s_or_b64 exec, exec, s[0:1]
	v_or_b32_e32 v146, 48, v176
	v_mov_b32_e32 v147, v177
	s_waitcnt lgkmcnt(0)
	v_lshlrev_b64 v[100:101], 12, v[146:147]
	s_waitcnt lgkmcnt(0)
	v_lshl_add_u64 v[100:101], v[184:185], 0, v[100:101]
	v_or_b32_e32 v118, 60, v176
	v_mov_b32_e32 v119, v177
	global_load_dwordx4 v[112:115], v[100:101], off nt
	v_lshl_add_u64 v[100:101], v[146:147], 3, s[10:11]
	v_or_b32_e32 v142, 52, v176
	v_mov_b32_e32 v143, v177
	v_lshl_add_u64 v[116:117], v[118:119], 3, s[10:11]
	global_load_dword v186, v[100:101], off offset:4
	global_load_dword v136, v[116:117], off offset:4
	v_lshlrev_b64 v[100:101], 12, v[142:143]
	v_lshl_add_u64 v[100:101], v[184:185], 0, v[100:101]
	global_load_dwordx4 v[108:111], v[100:101], off nt
	v_lshl_add_u64 v[100:101], v[142:143], 3, s[10:11]
	v_or_b32_e32 v138, 56, v176
	v_mov_b32_e32 v139, v177
	global_load_dword v144, v[100:101], off offset:4
	v_lshlrev_b64 v[100:101], 12, v[138:139]
	v_lshl_add_u64 v[100:101], v[184:185], 0, v[100:101]
	global_load_dwordx4 v[104:107], v[100:101], off nt
	v_lshl_add_u64 v[100:101], v[138:139], 3, s[10:11]
	global_load_dword v140, v[100:101], off offset:4
	v_lshlrev_b64 v[100:101], 12, v[118:119]
	v_lshl_add_u64 v[100:101], v[184:185], 0, v[100:101]
	global_load_dwordx4 v[100:103], v[100:101], off nt
	ds_write_b128 v216, v[84:87]
	ds_write_b128 v217, v[88:91]
	ds_write_b128 v218, v[92:95]
	ds_write_b128 v219, v[96:99]
	s_waitcnt lgkmcnt(0)
	ds_read_b128 v[84:87], v220
	s_waitcnt vmcnt(18) lgkmcnt(0)
	v_pk_mul_f32 v[84:85], v[204:205], v[84:85] op_sel_hi:[0,1]
	v_pk_fma_f32 v[84:85], v[178:179], v[84:85], v[132:133]
	v_pk_mul_f32 v[86:87], v[204:205], v[86:87] op_sel_hi:[0,1]
	v_pk_fma_f32 v[86:87], v[180:181], v[86:87], v[134:135]
	v_pk_mul_f32 v[88:89], v[84:85], v[84:85]
	v_pk_mul_f32 v[90:91], v[86:87], v[86:87]
	v_add_f32_e32 v88, v88, v89
	v_add_f32_e32 v88, v90, v88
	v_add_f32_e32 v88, v91, v88
	s_nop 1
	v_mov_b32_dpp v89, v88 row_ror:8 row_mask:0xf bank_mask:0xf
	s_waitcnt lgkmcnt(0)
	v_add_f32_e32 v88, v88, v89
	s_nop 1
	v_mov_b32_dpp v89, v88 row_ror:4 row_mask:0xf bank_mask:0xf
	s_waitcnt lgkmcnt(0)
	v_add_f32_e32 v90, v88, v89
	s_nop 1
	v_mov_b32_dpp v91, v90 quad_perm:[2,3,0,1] row_mask:0xf bank_mask:0xf
	v_cvt_pk_bf16_f32 v88, v84, v85
	v_cvt_pk_bf16_f32 v89, v86, v87
	v_lshlrev_b64 v[86:87], 11, v[200:201]
	v_lshl_add_u64 v[86:87], s[24:25], 0, v[86:87]
	s_waitcnt lgkmcnt(0)
	v_add_f32_e32 v84, v90, v91
	s_nop 1
	v_mov_b32_dpp v85, v84 quad_perm:[1,0,3,2] row_mask:0xf bank_mask:0xf
	v_lshl_add_u64 v[86:87], v[86:87], 0, v[2:3]
	global_store_dwordx2 v[86:87], v[88:89], off
	s_and_saveexec_b64 s[0:1], vcc
	s_cbranch_execz .LBB0_551
	v_lshlrev_b64 v[86:87], 6, v[200:201]
	v_lshl_add_u64 v[86:87], s[6:7], 0, v[86:87]
	v_lshl_add_u64 v[86:87], s[22:23], 2, v[86:87]
	v_mov_b32_e32 v183, v3
	v_lshl_add_u64 v[86:87], v[86:87], 0, v[182:183]
	s_waitcnt lgkmcnt(0)
	v_add_f32_e32 v84, v84, v85
	global_store_dword v[86:87], v84, off
.LBB0_551:
	s_or_b64 exec, exec, s[0:1]
	s_waitcnt lgkmcnt(0)
	ds_read_b128 v[84:87], v221
	s_waitcnt vmcnt(16) lgkmcnt(0)
	v_pk_mul_f32 v[84:85], v[158:159], v[84:85] op_sel_hi:[0,1]
	v_pk_mul_f32 v[86:87], v[158:159], v[86:87] op_sel_hi:[0,1]
	v_pk_fma_f32 v[84:85], v[178:179], v[84:85], v[128:129]
	v_pk_fma_f32 v[86:87], v[180:181], v[86:87], v[130:131]
	v_pk_mul_f32 v[88:89], v[84:85], v[84:85]
	v_pk_mul_f32 v[90:91], v[86:87], v[86:87]
	v_add_f32_e32 v88, v88, v89
	v_add_f32_e32 v88, v90, v88
	v_add_f32_e32 v88, v91, v88
	s_nop 1
	v_mov_b32_dpp v89, v88 row_ror:8 row_mask:0xf bank_mask:0xf
	s_waitcnt lgkmcnt(0)
	v_add_f32_e32 v88, v88, v89
	s_nop 1
	v_mov_b32_dpp v89, v88 row_ror:4 row_mask:0xf bank_mask:0xf
	s_waitcnt lgkmcnt(0)
	v_add_f32_e32 v90, v88, v89
	s_nop 1
	v_mov_b32_dpp v91, v90 quad_perm:[2,3,0,1] row_mask:0xf bank_mask:0xf
	v_cvt_pk_bf16_f32 v88, v84, v85
	v_cvt_pk_bf16_f32 v89, v86, v87
	v_lshlrev_b64 v[86:87], 11, v[156:157]
	v_lshl_add_u64 v[86:87], s[24:25], 0, v[86:87]
	s_waitcnt lgkmcnt(0)
	v_add_f32_e32 v84, v90, v91
	s_nop 1
	v_mov_b32_dpp v85, v84 quad_perm:[1,0,3,2] row_mask:0xf bank_mask:0xf
	v_lshl_add_u64 v[86:87], v[86:87], 0, v[2:3]
	global_store_dwordx2 v[86:87], v[88:89], off
	s_and_saveexec_b64 s[0:1], vcc
	s_cbranch_execz .LBB0_553
	v_lshlrev_b64 v[86:87], 6, v[156:157]
	v_lshl_add_u64 v[86:87], s[6:7], 0, v[86:87]
	v_lshl_add_u64 v[86:87], s[22:23], 2, v[86:87]
	v_mov_b32_e32 v183, v3
	v_lshl_add_u64 v[86:87], v[86:87], 0, v[182:183]
	s_waitcnt lgkmcnt(0)
	v_add_f32_e32 v84, v84, v85
	global_store_dword v[86:87], v84, off
; __device__ __forceinline__ uint2 pack4(f32x4 v) { uint2 r; r.x = pack2(v[0], v[1]); r.y = pack2(v[2], v[3]); return r; }
;     __device__ __forceinline__ void epilogue(f32x4 (&acc)[8][4], const Desc& d, unsigned char* stg) const {
;     ...
;         for (int m = 0; m < 8; ++m) {
;             float4 xc[4]; float fc[4];
; #pragma unroll
;             for (int i2 = 0; i2 < 4; ++i2) { xc[i2] = xn[i2]; fc[i2] = fn[i2]; }
;             if (m < 7) {
; #pragma unroll
;                 for (int i2 = 0; i2 < 4; ++i2) { xn[i2] = *(const float4*)(p.x + (rowb + (m + 1) * 16 + i2 * 4) * D + col); fn[i2] = p.rs[rowb + (m + 1) * 16 + i2 * 4].y; }
;             }
; #pragma unroll
;             for (int n = 0; n < 4; ++n) stgf_put(stg, n, acc[m][n], l15, gq);
;             asm volatile("s_waitcnt lgkmcnt(0)" ::: "memory");
; #pragma unroll
;             for (int i2 = 0; i2 < 4; ++i2) {
;                 const int rl = i2 * 4 + rsub;
;                 const size_t row = rowb + m * 16 + i2 * 4;
;                 const f32x4 v = stgf_get(stg, rl, c);
;                 const float fsm = fc[i2];
;                 const float4 xv = xc[i2];
;                 float4 r;
;                 r.x = xv.x + g1.x * (v[0] * fsm); r.y = xv.y + g1.y * (v[1] * fsm); r.z = xv.z + g1.z * (v[2] * fsm); r.w = xv.w + g1.w * (v[3] * fsm);
;                 *(uint2*)(p.x1 + row * D + col) = pack4((f32x4){r.x, r.y, r.z, r.w});
;                 float ss = r.x * r.x + r.y * r.y + r.z * r.z + r.w * r.w;
;                 ss += __shfl_xor(ss, 8); ss += __shfl_xor(ss, 4); ss += __shfl_xor(ss, 2); ss += __shfl_xor(ss, 1);
;                 if (c == 0) p.st2[row * 16 + nt * 4 + wc] = ss;
;             }
;             asm volatile("s_waitcnt lgkmcnt(0)" ::: "memory");
.LBB0_553:
	s_or_b64 exec, exec, s[0:1]
	s_waitcnt lgkmcnt(0)
	ds_read_b128 v[84:87], v159
	s_waitcnt vmcnt(15) lgkmcnt(0)
	v_pk_mul_f32 v[84:85], v[154:155], v[84:85] op_sel_hi:[0,1]
	v_pk_mul_f32 v[86:87], v[154:155], v[86:87] op_sel_hi:[0,1]
	v_pk_fma_f32 v[84:85], v[178:179], v[84:85], v[124:125]
	v_pk_fma_f32 v[86:87], v[180:181], v[86:87], v[126:127]
	v_pk_mul_f32 v[88:89], v[84:85], v[84:85]
	v_pk_mul_f32 v[90:91], v[86:87], v[86:87]
	v_add_f32_e32 v88, v88, v89
	v_add_f32_e32 v88, v90, v88
	v_add_f32_e32 v88, v91, v88
	s_nop 1
	v_mov_b32_dpp v89, v88 row_ror:8 row_mask:0xf bank_mask:0xf
	s_waitcnt lgkmcnt(0)
	v_add_f32_e32 v88, v88, v89
	s_nop 1
	v_mov_b32_dpp v89, v88 row_ror:4 row_mask:0xf bank_mask:0xf
	s_waitcnt lgkmcnt(0)
	v_add_f32_e32 v90, v88, v89
	s_nop 1
	v_mov_b32_dpp v91, v90 quad_perm:[2,3,0,1] row_mask:0xf bank_mask:0xf
	v_cvt_pk_bf16_f32 v88, v84, v85
	v_cvt_pk_bf16_f32 v89, v86, v87
	v_lshlrev_b64 v[86:87], 11, v[152:153]
	v_lshl_add_u64 v[86:87], s[24:25], 0, v[86:87]
	s_waitcnt lgkmcnt(0)
	v_add_f32_e32 v84, v90, v91
	s_nop 1
	v_mov_b32_dpp v85, v84 quad_perm:[1,0,3,2] row_mask:0xf bank_mask:0xf
	v_lshl_add_u64 v[86:87], v[86:87], 0, v[2:3]
	global_store_dwordx2 v[86:87], v[88:89], off
	s_and_saveexec_b64 s[0:1], vcc
	s_cbranch_execz .LBB0_555
	v_lshlrev_b64 v[86:87], 6, v[152:153]
	v_lshl_add_u64 v[86:87], s[6:7], 0, v[86:87]
	v_lshl_add_u64 v[86:87], s[22:23], 2, v[86:87]
	v_mov_b32_e32 v183, v3
	v_lshl_add_u64 v[86:87], v[86:87], 0, v[182:183]
	s_waitcnt lgkmcnt(0)
	v_add_f32_e32 v84, v84, v85
	global_store_dword v[86:87], v84, off
.LBB0_555:
	s_or_b64 exec, exec, s[0:1]
	s_waitcnt lgkmcnt(0)
	ds_read_b128 v[84:87], v151
	s_waitcnt lgkmcnt(0)
	v_pk_mul_f32 v[84:85], v[150:151], v[84:85] op_sel_hi:[0,1]
	v_pk_mul_f32 v[86:87], v[150:151], v[86:87] op_sel_hi:[0,1]
	s_waitcnt vmcnt(15)
	v_pk_fma_f32 v[84:85], v[178:179], v[84:85], v[120:121]
	v_pk_fma_f32 v[86:87], v[180:181], v[86:87], v[122:123]
	v_pk_mul_f32 v[88:89], v[84:85], v[84:85]
	v_pk_mul_f32 v[90:91], v[86:87], v[86:87]
	v_add_f32_e32 v88, v88, v89
	v_add_f32_e32 v88, v90, v88
	v_add_f32_e32 v88, v91, v88
	s_nop 1
	v_mov_b32_dpp v89, v88 row_ror:8 row_mask:0xf bank_mask:0xf
	s_waitcnt lgkmcnt(0)
	v_add_f32_e32 v88, v88, v89
	s_nop 1
	v_mov_b32_dpp v89, v88 row_ror:4 row_mask:0xf bank_mask:0xf
	s_waitcnt lgkmcnt(0)
	v_add_f32_e32 v90, v88, v89
	s_nop 1
	v_mov_b32_dpp v91, v90 quad_perm:[2,3,0,1] row_mask:0xf bank_mask:0xf
	v_cvt_pk_bf16_f32 v88, v84, v85
	v_cvt_pk_bf16_f32 v89, v86, v87
	v_lshlrev_b64 v[86:87], 11, v[148:149]
	v_lshl_add_u64 v[86:87], s[24:25], 0, v[86:87]
	s_waitcnt lgkmcnt(0)
	v_add_f32_e32 v84, v90, v91
	s_nop 1
	v_mov_b32_dpp v85, v84 quad_perm:[1,0,3,2] row_mask:0xf bank_mask:0xf
	v_lshl_add_u64 v[86:87], v[86:87], 0, v[2:3]
	global_store_dwordx2 v[86:87], v[88:89], off
	s_and_saveexec_b64 s[0:1], vcc
	s_cbranch_execz .LBB0_557
	v_lshlrev_b64 v[86:87], 6, v[148:149]
	v_lshl_add_u64 v[86:87], s[6:7], 0, v[86:87]
	v_lshl_add_u64 v[86:87], s[22:23], 2, v[86:87]
	v_mov_b32_e32 v183, v3
	v_lshl_add_u64 v[86:87], v[86:87], 0, v[182:183]
	s_waitcnt lgkmcnt(0)
	v_add_f32_e32 v84, v84, v85
	global_store_dword v[86:87], v84, off
.LBB0_557:
	s_or_b64 exec, exec, s[0:1]
	v_or_b32_e32 v130, 64, v176
	v_mov_b32_e32 v131, v177
	s_waitcnt lgkmcnt(0)
	v_lshlrev_b64 v[84:85], 12, v[130:131]
	s_waitcnt lgkmcnt(0)
	v_lshl_add_u64 v[84:85], v[184:185], 0, v[84:85]
	v_or_b32_e32 v116, 0x4c, v176
	v_mov_b32_e32 v117, v177
	global_load_dwordx4 v[96:99], v[84:85], off nt
	v_lshl_add_u64 v[84:85], v[130:131], 3, s[10:11]
	v_or_b32_e32 v126, 0x44, v176
	v_mov_b32_e32 v127, v177
	v_lshl_add_u64 v[120:121], v[116:117], 3, s[10:11]
	global_load_dword v132, v[84:85], off offset:4
	v_or_b32_e32 v122, 0x48, v176
	global_load_dword v120, v[120:121], off offset:4
	v_lshlrev_b64 v[84:85], 12, v[126:127]
	v_lshl_add_u64 v[84:85], v[184:185], 0, v[84:85]
	global_load_dwordx4 v[92:95], v[84:85], off nt
	v_lshl_add_u64 v[84:85], v[126:127], 3, s[10:11]
	v_mov_b32_e32 v123, v177
	global_load_dword v128, v[84:85], off offset:4
	v_lshlrev_b64 v[84:85], 12, v[122:123]
	v_lshl_add_u64 v[84:85], v[184:185], 0, v[84:85]
	global_load_dwordx4 v[88:91], v[84:85], off nt
	v_lshl_add_u64 v[84:85], v[122:123], 3, s[10:11]
	global_load_dword v124, v[84:85], off offset:4
	v_lshlrev_b64 v[84:85], 12, v[116:117]
	v_lshl_add_u64 v[84:85], v[184:185], 0, v[84:85]
	global_load_dwordx4 v[84:87], v[84:85], off nt
	ds_write_b128 v216, v[68:71]
	ds_write_b128 v217, v[72:75]
	ds_write_b128 v218, v[76:79]
	ds_write_b128 v219, v[80:83]
	s_waitcnt lgkmcnt(0)
	ds_read_b128 v[68:71], v220
	s_waitcnt vmcnt(18) lgkmcnt(0)
	v_pk_mul_f32 v[68:69], v[186:187], v[68:69] op_sel_hi:[0,1]
	v_pk_fma_f32 v[68:69], v[178:179], v[68:69], v[112:113]
	v_pk_mul_f32 v[70:71], v[186:187], v[70:71] op_sel_hi:[0,1]
	v_pk_fma_f32 v[70:71], v[180:181], v[70:71], v[114:115]
	v_pk_mul_f32 v[72:73], v[68:69], v[68:69]
	v_pk_mul_f32 v[74:75], v[70:71], v[70:71]
	v_add_f32_e32 v72, v72, v73
	v_add_f32_e32 v72, v74, v72
	v_add_f32_e32 v72, v75, v72
	s_nop 1
	v_mov_b32_dpp v73, v72 row_ror:8 row_mask:0xf bank_mask:0xf
	s_waitcnt lgkmcnt(0)
	v_add_f32_e32 v72, v72, v73
	s_nop 1
	v_mov_b32_dpp v73, v72 row_ror:4 row_mask:0xf bank_mask:0xf
	s_waitcnt lgkmcnt(0)
	v_add_f32_e32 v74, v72, v73
	s_nop 1
	v_mov_b32_dpp v75, v74 quad_perm:[2,3,0,1] row_mask:0xf bank_mask:0xf
	v_cvt_pk_bf16_f32 v72, v68, v69
	v_cvt_pk_bf16_f32 v73, v70, v71
	v_lshlrev_b64 v[70:71], 11, v[146:147]
	v_lshl_add_u64 v[70:71], s[24:25], 0, v[70:71]
	s_waitcnt lgkmcnt(0)
	v_add_f32_e32 v68, v74, v75
	s_nop 1
	v_mov_b32_dpp v69, v68 quad_perm:[1,0,3,2] row_mask:0xf bank_mask:0xf
	v_lshl_add_u64 v[70:71], v[70:71], 0, v[2:3]
	global_store_dwordx2 v[70:71], v[72:73], off
	s_and_saveexec_b64 s[0:1], vcc
	s_cbranch_execz .LBB0_559
	v_lshlrev_b64 v[70:71], 6, v[146:147]
	v_lshl_add_u64 v[70:71], s[6:7], 0, v[70:71]
	v_lshl_add_u64 v[70:71], s[22:23], 2, v[70:71]
	v_mov_b32_e32 v183, v3
	v_lshl_add_u64 v[70:71], v[70:71], 0, v[182:183]
	s_waitcnt lgkmcnt(0)
	v_add_f32_e32 v68, v68, v69
	global_store_dword v[70:71], v68, off
; __device__ __forceinline__ uint2 pack4(f32x4 v) { uint2 r; r.x = pack2(v[0], v[1]); r.y = pack2(v[2], v[3]); return r; }
;     __device__ __forceinline__ void epilogue(f32x4 (&acc)[8][4], const Desc& d, unsigned char* stg) const {
;     ...
;         for (int m = 0; m < 8; ++m) {
;             float4 xc[4]; float fc[4];
; #pragma unroll
;             for (int i2 = 0; i2 < 4; ++i2) { xc[i2] = xn[i2]; fc[i2] = fn[i2]; }
;             if (m < 7) {
; #pragma unroll
;                 for (int i2 = 0; i2 < 4; ++i2) { xn[i2] = *(const float4*)(p.x + (rowb + (m + 1) * 16 + i2 * 4) * D + col); fn[i2] = p.rs[rowb + (m + 1) * 16 + i2 * 4].y; }
;             }
; #pragma unroll
;             for (int n = 0; n < 4; ++n) stgf_put(stg, n, acc[m][n], l15, gq);
;             asm volatile("s_waitcnt lgkmcnt(0)" ::: "memory");
; #pragma unroll
;             for (int i2 = 0; i2 < 4; ++i2) {
;                 const int rl = i2 * 4 + rsub;
;                 const size_t row = rowb + m * 16 + i2 * 4;
;                 const f32x4 v = stgf_get(stg, rl, c);
;                 const float fsm = fc[i2];
;                 const float4 xv = xc[i2];
;                 float4 r;
;                 r.x = xv.x + g1.x * (v[0] * fsm); r.y = xv.y + g1.y * (v[1] * fsm); r.z = xv.z + g1.z * (v[2] * fsm); r.w = xv.w + g1.w * (v[3] * fsm);
;                 *(uint2*)(p.x1 + row * D + col) = pack4((f32x4){r.x, r.y, r.z, r.w});
;                 float ss = r.x * r.x + r.y * r.y + r.z * r.z + r.w * r.w;
;                 ss += __shfl_xor(ss, 8); ss += __shfl_xor(ss, 4); ss += __shfl_xor(ss, 2); ss += __shfl_xor(ss, 1);
;                 if (c == 0) p.st2[row * 16 + nt * 4 + wc] = ss;
;             }
;             asm volatile("s_waitcnt lgkmcnt(0)" ::: "memory");
.LBB0_559:
	s_or_b64 exec, exec, s[0:1]
	s_waitcnt lgkmcnt(0)
	ds_read_b128 v[68:71], v221
	s_waitcnt vmcnt(16) lgkmcnt(0)
	v_pk_mul_f32 v[68:69], v[144:145], v[68:69] op_sel_hi:[0,1]
	v_pk_mul_f32 v[70:71], v[144:145], v[70:71] op_sel_hi:[0,1]
	v_pk_fma_f32 v[68:69], v[178:179], v[68:69], v[108:109]
	v_pk_fma_f32 v[70:71], v[180:181], v[70:71], v[110:111]
	v_pk_mul_f32 v[72:73], v[68:69], v[68:69]
	v_pk_mul_f32 v[74:75], v[70:71], v[70:71]
	v_add_f32_e32 v72, v72, v73
	v_add_f32_e32 v72, v74, v72
	v_add_f32_e32 v72, v75, v72
	s_nop 1
	v_mov_b32_dpp v73, v72 row_ror:8 row_mask:0xf bank_mask:0xf
	s_waitcnt lgkmcnt(0)
	v_add_f32_e32 v72, v72, v73
	s_nop 1
	v_mov_b32_dpp v73, v72 row_ror:4 row_mask:0xf bank_mask:0xf
	s_waitcnt lgkmcnt(0)
	v_add_f32_e32 v74, v72, v73
	s_nop 1
	v_mov_b32_dpp v75, v74 quad_perm:[2,3,0,1] row_mask:0xf bank_mask:0xf
	v_cvt_pk_bf16_f32 v72, v68, v69
	v_cvt_pk_bf16_f32 v73, v70, v71
	v_lshlrev_b64 v[70:71], 11, v[142:143]
	v_lshl_add_u64 v[70:71], s[24:25], 0, v[70:71]
	s_waitcnt lgkmcnt(0)
	v_add_f32_e32 v68, v74, v75
	s_nop 1
	v_mov_b32_dpp v69, v68 quad_perm:[1,0,3,2] row_mask:0xf bank_mask:0xf
	v_lshl_add_u64 v[70:71], v[70:71], 0, v[2:3]
	global_store_dwordx2 v[70:71], v[72:73], off
	s_and_saveexec_b64 s[0:1], vcc
	s_cbranch_execz .LBB0_561
	v_lshlrev_b64 v[70:71], 6, v[142:143]
	v_lshl_add_u64 v[70:71], s[6:7], 0, v[70:71]
	v_lshl_add_u64 v[70:71], s[22:23], 2, v[70:71]
	v_mov_b32_e32 v183, v3
	v_lshl_add_u64 v[70:71], v[70:71], 0, v[182:183]
	s_waitcnt lgkmcnt(0)
	v_add_f32_e32 v68, v68, v69
	global_store_dword v[70:71], v68, off
.LBB0_561:
	s_or_b64 exec, exec, s[0:1]
	s_waitcnt lgkmcnt(0)
	ds_read_b128 v[68:71], v159
	s_waitcnt vmcnt(15) lgkmcnt(0)
	v_pk_mul_f32 v[68:69], v[140:141], v[68:69] op_sel_hi:[0,1]
	v_pk_mul_f32 v[70:71], v[140:141], v[70:71] op_sel_hi:[0,1]
	v_pk_fma_f32 v[68:69], v[178:179], v[68:69], v[104:105]
	v_pk_fma_f32 v[70:71], v[180:181], v[70:71], v[106:107]
	v_pk_mul_f32 v[72:73], v[68:69], v[68:69]
	v_pk_mul_f32 v[74:75], v[70:71], v[70:71]
	v_add_f32_e32 v72, v72, v73
	v_add_f32_e32 v72, v74, v72
	v_add_f32_e32 v72, v75, v72
	s_nop 1
	v_mov_b32_dpp v73, v72 row_ror:8 row_mask:0xf bank_mask:0xf
	s_waitcnt lgkmcnt(0)
	v_add_f32_e32 v72, v72, v73
	s_nop 1
	v_mov_b32_dpp v73, v72 row_ror:4 row_mask:0xf bank_mask:0xf
	s_waitcnt lgkmcnt(0)
	v_add_f32_e32 v74, v72, v73
	s_nop 1
	v_mov_b32_dpp v75, v74 quad_perm:[2,3,0,1] row_mask:0xf bank_mask:0xf
	v_cvt_pk_bf16_f32 v72, v68, v69
	v_cvt_pk_bf16_f32 v73, v70, v71
	v_lshlrev_b64 v[70:71], 11, v[138:139]
	v_lshl_add_u64 v[70:71], s[24:25], 0, v[70:71]
	s_waitcnt lgkmcnt(0)
	v_add_f32_e32 v68, v74, v75
	s_nop 1
	v_mov_b32_dpp v69, v68 quad_perm:[1,0,3,2] row_mask:0xf bank_mask:0xf
	v_lshl_add_u64 v[70:71], v[70:71], 0, v[2:3]
	global_store_dwordx2 v[70:71], v[72:73], off
	s_and_saveexec_b64 s[0:1], vcc
	s_cbranch_execz .LBB0_563
	v_lshlrev_b64 v[70:71], 6, v[138:139]
	v_lshl_add_u64 v[70:71], s[6:7], 0, v[70:71]
	v_lshl_add_u64 v[70:71], s[22:23], 2, v[70:71]
	v_mov_b32_e32 v183, v3
	v_lshl_add_u64 v[70:71], v[70:71], 0, v[182:183]
	s_waitcnt lgkmcnt(0)
	v_add_f32_e32 v68, v68, v69
	global_store_dword v[70:71], v68, off
.LBB0_563:
	s_or_b64 exec, exec, s[0:1]
	s_waitcnt lgkmcnt(0)
	ds_read_b128 v[68:71], v151
	s_waitcnt lgkmcnt(0)
	v_pk_mul_f32 v[68:69], v[136:137], v[68:69] op_sel_hi:[0,1]
	v_pk_mul_f32 v[70:71], v[136:137], v[70:71] op_sel_hi:[0,1]
	s_waitcnt vmcnt(15)
	v_pk_fma_f32 v[68:69], v[178:179], v[68:69], v[100:101]
	v_pk_fma_f32 v[70:71], v[180:181], v[70:71], v[102:103]
	v_pk_mul_f32 v[72:73], v[68:69], v[68:69]
	v_pk_mul_f32 v[74:75], v[70:71], v[70:71]
	v_add_f32_e32 v72, v72, v73
	v_add_f32_e32 v72, v74, v72
	v_add_f32_e32 v72, v75, v72
	s_nop 1
	v_mov_b32_dpp v73, v72 row_ror:8 row_mask:0xf bank_mask:0xf
	s_waitcnt lgkmcnt(0)
	v_add_f32_e32 v72, v72, v73
	s_nop 1
	v_mov_b32_dpp v73, v72 row_ror:4 row_mask:0xf bank_mask:0xf
	s_waitcnt lgkmcnt(0)
	v_add_f32_e32 v74, v72, v73
	s_nop 1
	v_mov_b32_dpp v75, v74 quad_perm:[2,3,0,1] row_mask:0xf bank_mask:0xf
	v_cvt_pk_bf16_f32 v72, v68, v69
	v_cvt_pk_bf16_f32 v73, v70, v71
	v_lshlrev_b64 v[70:71], 11, v[118:119]
	v_lshl_add_u64 v[70:71], s[24:25], 0, v[70:71]
	s_waitcnt lgkmcnt(0)
	v_add_f32_e32 v68, v74, v75
	s_nop 1
	v_mov_b32_dpp v69, v68 quad_perm:[1,0,3,2] row_mask:0xf bank_mask:0xf
	v_lshl_add_u64 v[70:71], v[70:71], 0, v[2:3]
	global_store_dwordx2 v[70:71], v[72:73], off
	s_and_saveexec_b64 s[0:1], vcc
	s_cbranch_execz .LBB0_565
	v_lshlrev_b64 v[70:71], 6, v[118:119]
	v_lshl_add_u64 v[70:71], s[6:7], 0, v[70:71]
	v_lshl_add_u64 v[70:71], s[22:23], 2, v[70:71]
	v_mov_b32_e32 v183, v3
	v_lshl_add_u64 v[70:71], v[70:71], 0, v[182:183]
	s_waitcnt lgkmcnt(0)
	v_add_f32_e32 v68, v68, v69
	global_store_dword v[70:71], v68, off
; __device__ __forceinline__ uint2 pack4(f32x4 v) { uint2 r; r.x = pack2(v[0], v[1]); r.y = pack2(v[2], v[3]); return r; }
;     __device__ __forceinline__ void epilogue(f32x4 (&acc)[8][4], const Desc& d, unsigned char* stg) const {
;     ...
;         for (int m = 0; m < 8; ++m) {
;             float4 xc[4]; float fc[4];
; #pragma unroll
;             for (int i2 = 0; i2 < 4; ++i2) { xc[i2] = xn[i2]; fc[i2] = fn[i2]; }
;             if (m < 7) {
; #pragma unroll
;                 for (int i2 = 0; i2 < 4; ++i2) { xn[i2] = *(const float4*)(p.x + (rowb + (m + 1) * 16 + i2 * 4) * D + col); fn[i2] = p.rs[rowb + (m + 1) * 16 + i2 * 4].y; }
;             }
; #pragma unroll
;             for (int n = 0; n < 4; ++n) stgf_put(stg, n, acc[m][n], l15, gq);
;             asm volatile("s_waitcnt lgkmcnt(0)" ::: "memory");
; #pragma unroll
;             for (int i2 = 0; i2 < 4; ++i2) {
;                 const int rl = i2 * 4 + rsub;
;                 const size_t row = rowb + m * 16 + i2 * 4;
;                 const f32x4 v = stgf_get(stg, rl, c);
;                 const float fsm = fc[i2];
;                 const float4 xv = xc[i2];
;                 float4 r;
;                 r.x = xv.x + g1.x * (v[0] * fsm); r.y = xv.y + g1.y * (v[1] * fsm); r.z = xv.z + g1.z * (v[2] * fsm); r.w = xv.w + g1.w * (v[3] * fsm);
;                 *(uint2*)(p.x1 + row * D + col) = pack4((f32x4){r.x, r.y, r.z, r.w});
;                 float ss = r.x * r.x + r.y * r.y + r.z * r.z + r.w * r.w;
;                 ss += __shfl_xor(ss, 8); ss += __shfl_xor(ss, 4); ss += __shfl_xor(ss, 2); ss += __shfl_xor(ss, 1);
;                 if (c == 0) p.st2[row * 16 + nt * 4 + wc] = ss;
;             }
;             asm volatile("s_waitcnt lgkmcnt(0)" ::: "memory");
.LBB0_565:
	s_or_b64 exec, exec, s[0:1]
	v_or_b32_e32 v112, 0x50, v176
	v_mov_b32_e32 v113, v177
	s_waitcnt lgkmcnt(0)
	v_lshlrev_b64 v[68:69], 12, v[112:113]
	s_waitcnt lgkmcnt(0)
	v_lshl_add_u64 v[68:69], v[184:185], 0, v[68:69]
	v_or_b32_e32 v100, 0x5c, v176
	v_mov_b32_e32 v101, v177
	global_load_dwordx4 v[80:83], v[68:69], off nt
	v_lshl_add_u64 v[68:69], v[112:113], 3, s[10:11]
	v_or_b32_e32 v108, 0x54, v176
	v_mov_b32_e32 v109, v177
	v_lshl_add_u64 v[102:103], v[100:101], 3, s[10:11]
	global_load_dword v114, v[68:69], off offset:4
	v_or_b32_e32 v104, 0x58, v176
	global_load_dword v102, v[102:103], off offset:4
	v_lshlrev_b64 v[68:69], 12, v[108:109]
	v_lshl_add_u64 v[68:69], v[184:185], 0, v[68:69]
	global_load_dwordx4 v[76:79], v[68:69], off nt
	v_lshl_add_u64 v[68:69], v[108:109], 3, s[10:11]
	v_mov_b32_e32 v105, v177
	global_load_dword v110, v[68:69], off offset:4
	v_lshlrev_b64 v[68:69], 12, v[104:105]
	v_lshl_add_u64 v[68:69], v[184:185], 0, v[68:69]
	global_load_dwordx4 v[72:75], v[68:69], off nt
	v_lshl_add_u64 v[68:69], v[104:105], 3, s[10:11]
	global_load_dword v106, v[68:69], off offset:4
	v_lshlrev_b64 v[68:69], 12, v[100:101]
	v_lshl_add_u64 v[68:69], v[184:185], 0, v[68:69]
	global_load_dwordx4 v[68:71], v[68:69], off nt
	ds_write_b128 v216, v[52:55]
	ds_write_b128 v217, v[56:59]
	ds_write_b128 v218, v[60:63]
	ds_write_b128 v219, v[64:67]
	s_waitcnt lgkmcnt(0)
	ds_read_b128 v[52:55], v220
	s_waitcnt vmcnt(18) lgkmcnt(0)
	v_pk_mul_f32 v[52:53], v[132:133], v[52:53] op_sel_hi:[0,1]
	v_pk_fma_f32 v[52:53], v[178:179], v[52:53], v[96:97]
	v_pk_mul_f32 v[54:55], v[132:133], v[54:55] op_sel_hi:[0,1]
	v_pk_fma_f32 v[54:55], v[180:181], v[54:55], v[98:99]
	v_pk_mul_f32 v[56:57], v[52:53], v[52:53]
	v_pk_mul_f32 v[58:59], v[54:55], v[54:55]
	v_add_f32_e32 v56, v56, v57
	v_add_f32_e32 v56, v58, v56
	v_add_f32_e32 v56, v59, v56
	s_nop 1
	v_mov_b32_dpp v57, v56 row_ror:8 row_mask:0xf bank_mask:0xf
	s_waitcnt lgkmcnt(0)
	v_add_f32_e32 v56, v56, v57
	s_nop 1
	v_mov_b32_dpp v57, v56 row_ror:4 row_mask:0xf bank_mask:0xf
	s_waitcnt lgkmcnt(0)
	v_add_f32_e32 v58, v56, v57
	s_nop 1
	v_mov_b32_dpp v59, v58 quad_perm:[2,3,0,1] row_mask:0xf bank_mask:0xf
	v_cvt_pk_bf16_f32 v56, v52, v53
	v_cvt_pk_bf16_f32 v57, v54, v55
	v_lshlrev_b64 v[54:55], 11, v[130:131]
	v_lshl_add_u64 v[54:55], s[24:25], 0, v[54:55]
	s_waitcnt lgkmcnt(0)
	v_add_f32_e32 v52, v58, v59
	s_nop 1
	v_mov_b32_dpp v53, v52 quad_perm:[1,0,3,2] row_mask:0xf bank_mask:0xf
	v_lshl_add_u64 v[54:55], v[54:55], 0, v[2:3]
	global_store_dwordx2 v[54:55], v[56:57], off
	s_and_saveexec_b64 s[0:1], vcc
	s_cbranch_execz .LBB0_567
	v_lshlrev_b64 v[54:55], 6, v[130:131]
	v_lshl_add_u64 v[54:55], s[6:7], 0, v[54:55]
	v_lshl_add_u64 v[54:55], s[22:23], 2, v[54:55]
	v_mov_b32_e32 v183, v3
	v_lshl_add_u64 v[54:55], v[54:55], 0, v[182:183]
	s_waitcnt lgkmcnt(0)
	v_add_f32_e32 v52, v52, v53
	global_store_dword v[54:55], v52, off
.LBB0_567:
	s_or_b64 exec, exec, s[0:1]
	s_waitcnt lgkmcnt(0)
	ds_read_b128 v[52:55], v221
	s_waitcnt vmcnt(16) lgkmcnt(0)
	v_pk_mul_f32 v[52:53], v[128:129], v[52:53] op_sel_hi:[0,1]
	v_pk_mul_f32 v[54:55], v[128:129], v[54:55] op_sel_hi:[0,1]
	v_pk_fma_f32 v[52:53], v[178:179], v[52:53], v[92:93]
	v_pk_fma_f32 v[54:55], v[180:181], v[54:55], v[94:95]
	v_pk_mul_f32 v[56:57], v[52:53], v[52:53]
	v_pk_mul_f32 v[58:59], v[54:55], v[54:55]
	v_add_f32_e32 v56, v56, v57
	v_add_f32_e32 v56, v58, v56
	v_add_f32_e32 v56, v59, v56
	s_nop 1
	v_mov_b32_dpp v57, v56 row_ror:8 row_mask:0xf bank_mask:0xf
	s_waitcnt lgkmcnt(0)
	v_add_f32_e32 v56, v56, v57
	s_nop 1
	v_mov_b32_dpp v57, v56 row_ror:4 row_mask:0xf bank_mask:0xf
	s_waitcnt lgkmcnt(0)
	v_add_f32_e32 v58, v56, v57
	s_nop 1
	v_mov_b32_dpp v59, v58 quad_perm:[2,3,0,1] row_mask:0xf bank_mask:0xf
	v_cvt_pk_bf16_f32 v56, v52, v53
	v_cvt_pk_bf16_f32 v57, v54, v55
	v_lshlrev_b64 v[54:55], 11, v[126:127]
	v_lshl_add_u64 v[54:55], s[24:25], 0, v[54:55]
	s_waitcnt lgkmcnt(0)
	v_add_f32_e32 v52, v58, v59
	s_nop 1
	v_mov_b32_dpp v53, v52 quad_perm:[1,0,3,2] row_mask:0xf bank_mask:0xf
	v_lshl_add_u64 v[54:55], v[54:55], 0, v[2:3]
	global_store_dwordx2 v[54:55], v[56:57], off
	s_and_saveexec_b64 s[0:1], vcc
	s_cbranch_execz .LBB0_569
	v_lshlrev_b64 v[54:55], 6, v[126:127]
	v_lshl_add_u64 v[54:55], s[6:7], 0, v[54:55]
	v_lshl_add_u64 v[54:55], s[22:23], 2, v[54:55]
	v_mov_b32_e32 v183, v3
	v_lshl_add_u64 v[54:55], v[54:55], 0, v[182:183]
	s_waitcnt lgkmcnt(0)
	v_add_f32_e32 v52, v52, v53
	global_store_dword v[54:55], v52, off
.LBB0_569:
	s_or_b64 exec, exec, s[0:1]
	s_waitcnt lgkmcnt(0)
	ds_read_b128 v[52:55], v159
	s_waitcnt vmcnt(15) lgkmcnt(0)
	v_pk_mul_f32 v[52:53], v[124:125], v[52:53] op_sel_hi:[0,1]
	v_pk_mul_f32 v[54:55], v[124:125], v[54:55] op_sel_hi:[0,1]
	v_pk_fma_f32 v[52:53], v[178:179], v[52:53], v[88:89]
	v_pk_fma_f32 v[54:55], v[180:181], v[54:55], v[90:91]
	v_pk_mul_f32 v[56:57], v[52:53], v[52:53]
	v_pk_mul_f32 v[58:59], v[54:55], v[54:55]
	v_add_f32_e32 v56, v56, v57
	v_add_f32_e32 v56, v58, v56
	v_add_f32_e32 v56, v59, v56
	s_nop 1
	v_mov_b32_dpp v57, v56 row_ror:8 row_mask:0xf bank_mask:0xf
	s_waitcnt lgkmcnt(0)
	v_add_f32_e32 v56, v56, v57
	s_nop 1
	v_mov_b32_dpp v57, v56 row_ror:4 row_mask:0xf bank_mask:0xf
	s_waitcnt lgkmcnt(0)
	v_add_f32_e32 v58, v56, v57
	s_nop 1
	v_mov_b32_dpp v59, v58 quad_perm:[2,3,0,1] row_mask:0xf bank_mask:0xf
	v_cvt_pk_bf16_f32 v56, v52, v53
	v_cvt_pk_bf16_f32 v57, v54, v55
	v_lshlrev_b64 v[54:55], 11, v[122:123]
	v_lshl_add_u64 v[54:55], s[24:25], 0, v[54:55]
	s_waitcnt lgkmcnt(0)
	v_add_f32_e32 v52, v58, v59
	s_nop 1
	v_mov_b32_dpp v53, v52 quad_perm:[1,0,3,2] row_mask:0xf bank_mask:0xf
	v_lshl_add_u64 v[54:55], v[54:55], 0, v[2:3]
	global_store_dwordx2 v[54:55], v[56:57], off
	s_and_saveexec_b64 s[0:1], vcc
	s_cbranch_execz .LBB0_571
	v_lshlrev_b64 v[54:55], 6, v[122:123]
	v_lshl_add_u64 v[54:55], s[6:7], 0, v[54:55]
	v_lshl_add_u64 v[54:55], s[22:23], 2, v[54:55]
	v_mov_b32_e32 v183, v3
	v_lshl_add_u64 v[54:55], v[54:55], 0, v[182:183]
	s_waitcnt lgkmcnt(0)
	v_add_f32_e32 v52, v52, v53
	global_store_dword v[54:55], v52, off
; __device__ __forceinline__ uint2 pack4(f32x4 v) { uint2 r; r.x = pack2(v[0], v[1]); r.y = pack2(v[2], v[3]); return r; }
;     __device__ __forceinline__ void epilogue(f32x4 (&acc)[8][4], const Desc& d, unsigned char* stg) const {
;     ...
;         for (int m = 0; m < 8; ++m) {
;             float4 xc[4]; float fc[4];
; #pragma unroll
;             for (int i2 = 0; i2 < 4; ++i2) { xc[i2] = xn[i2]; fc[i2] = fn[i2]; }
;             if (m < 7) {
; #pragma unroll
;                 for (int i2 = 0; i2 < 4; ++i2) { xn[i2] = *(const float4*)(p.x + (rowb + (m + 1) * 16 + i2 * 4) * D + col); fn[i2] = p.rs[rowb + (m + 1) * 16 + i2 * 4].y; }
;             }
; #pragma unroll
;             for (int n = 0; n < 4; ++n) stgf_put(stg, n, acc[m][n], l15, gq);
;             asm volatile("s_waitcnt lgkmcnt(0)" ::: "memory");
; #pragma unroll
;             for (int i2 = 0; i2 < 4; ++i2) {
;                 const int rl = i2 * 4 + rsub;
;                 const size_t row = rowb + m * 16 + i2 * 4;
;                 const f32x4 v = stgf_get(stg, rl, c);
;                 const float fsm = fc[i2];
;                 const float4 xv = xc[i2];
;                 float4 r;
;                 r.x = xv.x + g1.x * (v[0] * fsm); r.y = xv.y + g1.y * (v[1] * fsm); r.z = xv.z + g1.z * (v[2] * fsm); r.w = xv.w + g1.w * (v[3] * fsm);
;                 *(uint2*)(p.x1 + row * D + col) = pack4((f32x4){r.x, r.y, r.z, r.w});
;                 float ss = r.x * r.x + r.y * r.y + r.z * r.z + r.w * r.w;
;                 ss += __shfl_xor(ss, 8); ss += __shfl_xor(ss, 4); ss += __shfl_xor(ss, 2); ss += __shfl_xor(ss, 1);
;                 if (c == 0) p.st2[row * 16 + nt * 4 + wc] = ss;
;             }
.LBB0_571:
	s_or_b64 exec, exec, s[0:1]
	s_waitcnt lgkmcnt(0)
	ds_read_b128 v[52:55], v151
	s_waitcnt lgkmcnt(0)
	v_pk_mul_f32 v[52:53], v[120:121], v[52:53] op_sel_hi:[0,1]
	v_pk_mul_f32 v[54:55], v[120:121], v[54:55] op_sel_hi:[0,1]
	s_waitcnt vmcnt(15)
	v_pk_fma_f32 v[52:53], v[178:179], v[52:53], v[84:85]
	v_pk_fma_f32 v[54:55], v[180:181], v[54:55], v[86:87]
	v_pk_mul_f32 v[56:57], v[52:53], v[52:53]
	v_pk_mul_f32 v[58:59], v[54:55], v[54:55]
	v_add_f32_e32 v56, v56, v57
	v_add_f32_e32 v56, v58, v56
	v_add_f32_e32 v56, v59, v56
	s_nop 1
	v_mov_b32_dpp v57, v56 row_ror:8 row_mask:0xf bank_mask:0xf
	s_waitcnt lgkmcnt(0)
	v_add_f32_e32 v56, v56, v57
	s_nop 1
	v_mov_b32_dpp v57, v56 row_ror:4 row_mask:0xf bank_mask:0xf
	s_waitcnt lgkmcnt(0)
	v_add_f32_e32 v58, v56, v57
	s_nop 1
	v_mov_b32_dpp v59, v58 quad_perm:[2,3,0,1] row_mask:0xf bank_mask:0xf
	v_cvt_pk_bf16_f32 v56, v52, v53
	v_cvt_pk_bf16_f32 v57, v54, v55
	v_lshlrev_b64 v[54:55], 11, v[116:117]
	v_lshl_add_u64 v[54:55], s[24:25], 0, v[54:55]
	s_waitcnt lgkmcnt(0)
	v_add_f32_e32 v52, v58, v59
	s_nop 1
	v_mov_b32_dpp v53, v52 quad_perm:[1,0,3,2] row_mask:0xf bank_mask:0xf
	v_lshl_add_u64 v[54:55], v[54:55], 0, v[2:3]
	global_store_dwordx2 v[54:55], v[56:57], off
	s_and_saveexec_b64 s[0:1], vcc
	s_cbranch_execz .LBB0_573
	v_lshlrev_b64 v[54:55], 6, v[116:117]
	v_lshl_add_u64 v[54:55], s[6:7], 0, v[54:55]
	v_lshl_add_u64 v[54:55], s[22:23], 2, v[54:55]
	v_mov_b32_e32 v183, v3
	v_lshl_add_u64 v[54:55], v[54:55], 0, v[182:183]
	s_waitcnt lgkmcnt(0)
	v_add_f32_e32 v52, v52, v53
	global_store_dword v[54:55], v52, off
.LBB0_573:
	s_or_b64 exec, exec, s[0:1]
	v_or_b32_e32 v96, 0x60, v176
	v_mov_b32_e32 v97, v177
	s_waitcnt lgkmcnt(0)
	v_lshlrev_b64 v[52:53], 12, v[96:97]
	s_waitcnt lgkmcnt(0)
	v_lshl_add_u64 v[52:53], v[184:185], 0, v[52:53]
	v_or_b32_e32 v84, 0x6c, v176
	v_mov_b32_e32 v85, v177
	global_load_dwordx4 v[64:67], v[52:53], off nt
	v_lshl_add_u64 v[52:53], v[96:97], 3, s[10:11]
	v_or_b32_e32 v92, 0x64, v176
	v_mov_b32_e32 v93, v177
	v_lshl_add_u64 v[86:87], v[84:85], 3, s[10:11]
	global_load_dword v98, v[52:53], off offset:4
	v_or_b32_e32 v88, 0x68, v176
	global_load_dword v86, v[86:87], off offset:4
	v_lshlrev_b64 v[52:53], 12, v[92:93]
	v_lshl_add_u64 v[52:53], v[184:185], 0, v[52:53]
	global_load_dwordx4 v[60:63], v[52:53], off nt
	v_lshl_add_u64 v[52:53], v[92:93], 3, s[10:11]
	v_mov_b32_e32 v89, v177
	global_load_dword v94, v[52:53], off offset:4
	v_lshlrev_b64 v[52:53], 12, v[88:89]
	v_lshl_add_u64 v[52:53], v[184:185], 0, v[52:53]
	global_load_dwordx4 v[56:59], v[52:53], off nt
	v_lshl_add_u64 v[52:53], v[88:89], 3, s[10:11]
	global_load_dword v90, v[52:53], off offset:4
	v_lshlrev_b64 v[52:53], 12, v[84:85]
	v_lshl_add_u64 v[52:53], v[184:185], 0, v[52:53]
	global_load_dwordx4 v[52:55], v[52:53], off nt
	ds_write_b128 v216, v[36:39]
	ds_write_b128 v217, v[40:43]
	ds_write_b128 v218, v[44:47]
	ds_write_b128 v219, v[48:51]
	s_waitcnt lgkmcnt(0)
	ds_read_b128 v[36:39], v220
	s_waitcnt vmcnt(18) lgkmcnt(0)
	v_pk_mul_f32 v[36:37], v[114:115], v[36:37] op_sel_hi:[0,1]
	v_pk_fma_f32 v[36:37], v[178:179], v[36:37], v[80:81]
	v_pk_mul_f32 v[38:39], v[114:115], v[38:39] op_sel_hi:[0,1]
	v_pk_fma_f32 v[38:39], v[180:181], v[38:39], v[82:83]
	v_pk_mul_f32 v[40:41], v[36:37], v[36:37]
	v_pk_mul_f32 v[42:43], v[38:39], v[38:39]
	v_add_f32_e32 v40, v40, v41
	v_add_f32_e32 v40, v42, v40
	v_add_f32_e32 v40, v43, v40
	s_nop 1
	v_mov_b32_dpp v41, v40 row_ror:8 row_mask:0xf bank_mask:0xf
	s_waitcnt lgkmcnt(0)
	v_add_f32_e32 v40, v40, v41
	s_nop 1
	v_mov_b32_dpp v41, v40 row_ror:4 row_mask:0xf bank_mask:0xf
	s_waitcnt lgkmcnt(0)
	v_add_f32_e32 v42, v40, v41
	s_nop 1
	v_mov_b32_dpp v43, v42 quad_perm:[2,3,0,1] row_mask:0xf bank_mask:0xf
	v_cvt_pk_bf16_f32 v40, v36, v37
	v_cvt_pk_bf16_f32 v41, v38, v39
	v_lshlrev_b64 v[38:39], 11, v[112:113]
	v_lshl_add_u64 v[38:39], s[24:25], 0, v[38:39]
	s_waitcnt lgkmcnt(0)
	v_add_f32_e32 v36, v42, v43
	s_nop 1
	v_mov_b32_dpp v37, v36 quad_perm:[1,0,3,2] row_mask:0xf bank_mask:0xf
	v_lshl_add_u64 v[38:39], v[38:39], 0, v[2:3]
	global_store_dwordx2 v[38:39], v[40:41], off
	s_and_saveexec_b64 s[0:1], vcc
	s_cbranch_execz .LBB0_575
	v_lshlrev_b64 v[38:39], 6, v[112:113]
	v_lshl_add_u64 v[38:39], s[6:7], 0, v[38:39]
	v_lshl_add_u64 v[38:39], s[22:23], 2, v[38:39]
	v_mov_b32_e32 v183, v3
	v_lshl_add_u64 v[38:39], v[38:39], 0, v[182:183]
	s_waitcnt lgkmcnt(0)
	v_add_f32_e32 v36, v36, v37
	global_store_dword v[38:39], v36, off
.LBB0_575:
	s_or_b64 exec, exec, s[0:1]
	s_waitcnt lgkmcnt(0)
	ds_read_b128 v[36:39], v221
	s_waitcnt vmcnt(16) lgkmcnt(0)
	v_pk_mul_f32 v[36:37], v[110:111], v[36:37] op_sel_hi:[0,1]
	v_pk_mul_f32 v[38:39], v[110:111], v[38:39] op_sel_hi:[0,1]
	v_pk_fma_f32 v[36:37], v[178:179], v[36:37], v[76:77]
	v_pk_fma_f32 v[38:39], v[180:181], v[38:39], v[78:79]
	v_pk_mul_f32 v[40:41], v[36:37], v[36:37]
	v_pk_mul_f32 v[42:43], v[38:39], v[38:39]
	v_add_f32_e32 v40, v40, v41
	v_add_f32_e32 v40, v42, v40
	v_add_f32_e32 v40, v43, v40
	s_nop 1
	v_mov_b32_dpp v41, v40 row_ror:8 row_mask:0xf bank_mask:0xf
	s_waitcnt lgkmcnt(0)
	v_add_f32_e32 v40, v40, v41
	s_nop 1
	v_mov_b32_dpp v41, v40 row_ror:4 row_mask:0xf bank_mask:0xf
	s_waitcnt lgkmcnt(0)
	v_add_f32_e32 v42, v40, v41
	s_nop 1
	v_mov_b32_dpp v43, v42 quad_perm:[2,3,0,1] row_mask:0xf bank_mask:0xf
	v_cvt_pk_bf16_f32 v40, v36, v37
	v_cvt_pk_bf16_f32 v41, v38, v39
	v_lshlrev_b64 v[38:39], 11, v[108:109]
	v_lshl_add_u64 v[38:39], s[24:25], 0, v[38:39]
	s_waitcnt lgkmcnt(0)
	v_add_f32_e32 v36, v42, v43
	s_nop 1
	v_mov_b32_dpp v37, v36 quad_perm:[1,0,3,2] row_mask:0xf bank_mask:0xf
	v_lshl_add_u64 v[38:39], v[38:39], 0, v[2:3]
	global_store_dwordx2 v[38:39], v[40:41], off
	s_and_saveexec_b64 s[0:1], vcc
	s_cbranch_execz .LBB0_577
	v_lshlrev_b64 v[38:39], 6, v[108:109]
	v_lshl_add_u64 v[38:39], s[6:7], 0, v[38:39]
	v_lshl_add_u64 v[38:39], s[22:23], 2, v[38:39]
	v_mov_b32_e32 v183, v3
	v_lshl_add_u64 v[38:39], v[38:39], 0, v[182:183]
	s_waitcnt lgkmcnt(0)
	v_add_f32_e32 v36, v36, v37
	global_store_dword v[38:39], v36, off
; __device__ __forceinline__ uint2 pack4(f32x4 v) { uint2 r; r.x = pack2(v[0], v[1]); r.y = pack2(v[2], v[3]); return r; }
;     __device__ __forceinline__ void epilogue(f32x4 (&acc)[8][4], const Desc& d, unsigned char* stg) const {
;     ...
;         for (int m = 0; m < 8; ++m) {
;             float4 xc[4]; float fc[4];
; #pragma unroll
;             for (int i2 = 0; i2 < 4; ++i2) { xc[i2] = xn[i2]; fc[i2] = fn[i2]; }
;             if (m < 7) {
; #pragma unroll
;                 for (int i2 = 0; i2 < 4; ++i2) { xn[i2] = *(const float4*)(p.x + (rowb + (m + 1) * 16 + i2 * 4) * D + col); fn[i2] = p.rs[rowb + (m + 1) * 16 + i2 * 4].y; }
;             }
; #pragma unroll
;             for (int n = 0; n < 4; ++n) stgf_put(stg, n, acc[m][n], l15, gq);
;             asm volatile("s_waitcnt lgkmcnt(0)" ::: "memory");
; #pragma unroll
;             for (int i2 = 0; i2 < 4; ++i2) {
;                 const int rl = i2 * 4 + rsub;
;                 const size_t row = rowb + m * 16 + i2 * 4;
;                 const f32x4 v = stgf_get(stg, rl, c);
;                 const float fsm = fc[i2];
;                 const float4 xv = xc[i2];
;                 float4 r;
;                 r.x = xv.x + g1.x * (v[0] * fsm); r.y = xv.y + g1.y * (v[1] * fsm); r.z = xv.z + g1.z * (v[2] * fsm); r.w = xv.w + g1.w * (v[3] * fsm);
;                 *(uint2*)(p.x1 + row * D + col) = pack4((f32x4){r.x, r.y, r.z, r.w});
;                 float ss = r.x * r.x + r.y * r.y + r.z * r.z + r.w * r.w;
;                 ss += __shfl_xor(ss, 8); ss += __shfl_xor(ss, 4); ss += __shfl_xor(ss, 2); ss += __shfl_xor(ss, 1);
;                 if (c == 0) p.st2[row * 16 + nt * 4 + wc] = ss;
;             }
.LBB0_577:
	s_or_b64 exec, exec, s[0:1]
	s_waitcnt lgkmcnt(0)
	ds_read_b128 v[36:39], v159
	s_waitcnt vmcnt(15) lgkmcnt(0)
	v_pk_mul_f32 v[36:37], v[106:107], v[36:37] op_sel_hi:[0,1]
	v_pk_mul_f32 v[38:39], v[106:107], v[38:39] op_sel_hi:[0,1]
	v_pk_fma_f32 v[36:37], v[178:179], v[36:37], v[72:73]
	v_pk_fma_f32 v[38:39], v[180:181], v[38:39], v[74:75]
	v_pk_mul_f32 v[40:41], v[36:37], v[36:37]
	v_pk_mul_f32 v[42:43], v[38:39], v[38:39]
	v_add_f32_e32 v40, v40, v41
	v_add_f32_e32 v40, v42, v40
	v_add_f32_e32 v40, v43, v40
	s_nop 1
	v_mov_b32_dpp v41, v40 row_ror:8 row_mask:0xf bank_mask:0xf
	s_waitcnt lgkmcnt(0)
	v_add_f32_e32 v40, v40, v41
	s_nop 1
	v_mov_b32_dpp v41, v40 row_ror:4 row_mask:0xf bank_mask:0xf
	s_waitcnt lgkmcnt(0)
	v_add_f32_e32 v42, v40, v41
	s_nop 1
	v_mov_b32_dpp v43, v42 quad_perm:[2,3,0,1] row_mask:0xf bank_mask:0xf
	v_cvt_pk_bf16_f32 v40, v36, v37
	v_cvt_pk_bf16_f32 v41, v38, v39
	v_lshlrev_b64 v[38:39], 11, v[104:105]
	v_lshl_add_u64 v[38:39], s[24:25], 0, v[38:39]
	s_waitcnt lgkmcnt(0)
	v_add_f32_e32 v36, v42, v43
	s_nop 1
	v_mov_b32_dpp v37, v36 quad_perm:[1,0,3,2] row_mask:0xf bank_mask:0xf
	v_lshl_add_u64 v[38:39], v[38:39], 0, v[2:3]
	global_store_dwordx2 v[38:39], v[40:41], off
	s_and_saveexec_b64 s[0:1], vcc
	s_cbranch_execz .LBB0_579
	v_lshlrev_b64 v[38:39], 6, v[104:105]
	v_lshl_add_u64 v[38:39], s[6:7], 0, v[38:39]
	v_lshl_add_u64 v[38:39], s[22:23], 2, v[38:39]
	v_mov_b32_e32 v183, v3
	v_lshl_add_u64 v[38:39], v[38:39], 0, v[182:183]
	s_waitcnt lgkmcnt(0)
	v_add_f32_e32 v36, v36, v37
	global_store_dword v[38:39], v36, off
.LBB0_579:
	s_or_b64 exec, exec, s[0:1]
	s_waitcnt lgkmcnt(0)
	ds_read_b128 v[36:39], v151
	s_waitcnt lgkmcnt(0)
	v_pk_mul_f32 v[36:37], v[102:103], v[36:37] op_sel_hi:[0,1]
	v_pk_mul_f32 v[38:39], v[102:103], v[38:39] op_sel_hi:[0,1]
	s_waitcnt vmcnt(15)
	v_pk_fma_f32 v[36:37], v[178:179], v[36:37], v[68:69]
	v_pk_fma_f32 v[38:39], v[180:181], v[38:39], v[70:71]
	v_pk_mul_f32 v[40:41], v[36:37], v[36:37]
	v_pk_mul_f32 v[42:43], v[38:39], v[38:39]
	v_add_f32_e32 v40, v40, v41
	v_add_f32_e32 v40, v42, v40
	v_add_f32_e32 v40, v43, v40
	s_nop 1
	v_mov_b32_dpp v41, v40 row_ror:8 row_mask:0xf bank_mask:0xf
	s_waitcnt lgkmcnt(0)
	v_add_f32_e32 v40, v40, v41
	s_nop 1
	v_mov_b32_dpp v41, v40 row_ror:4 row_mask:0xf bank_mask:0xf
	s_waitcnt lgkmcnt(0)
	v_add_f32_e32 v42, v40, v41
	s_nop 1
	v_mov_b32_dpp v43, v42 quad_perm:[2,3,0,1] row_mask:0xf bank_mask:0xf
	v_cvt_pk_bf16_f32 v40, v36, v37
	v_cvt_pk_bf16_f32 v41, v38, v39
	v_lshlrev_b64 v[38:39], 11, v[100:101]
	v_lshl_add_u64 v[38:39], s[24:25], 0, v[38:39]
	s_waitcnt lgkmcnt(0)
	v_add_f32_e32 v36, v42, v43
	s_nop 1
	v_mov_b32_dpp v37, v36 quad_perm:[1,0,3,2] row_mask:0xf bank_mask:0xf
	v_lshl_add_u64 v[38:39], v[38:39], 0, v[2:3]
	global_store_dwordx2 v[38:39], v[40:41], off
	s_and_saveexec_b64 s[0:1], vcc
	s_cbranch_execz .LBB0_581
	v_lshlrev_b64 v[38:39], 6, v[100:101]
	v_lshl_add_u64 v[38:39], s[6:7], 0, v[38:39]
	v_lshl_add_u64 v[38:39], s[22:23], 2, v[38:39]
	v_mov_b32_e32 v183, v3
	v_lshl_add_u64 v[38:39], v[38:39], 0, v[182:183]
	s_waitcnt lgkmcnt(0)
	v_add_f32_e32 v36, v36, v37
	global_store_dword v[38:39], v36, off
.LBB0_581:
	s_or_b64 exec, exec, s[0:1]
	v_or_b32_e32 v78, 0x70, v176
	v_mov_b32_e32 v79, v177
	s_waitcnt lgkmcnt(0)
	v_lshlrev_b64 v[36:37], 12, v[78:79]
	s_waitcnt lgkmcnt(0)
	v_lshl_add_u64 v[36:37], v[184:185], 0, v[36:37]
	v_or_b32_e32 v74, 0x74, v176
	v_or_b32_e32 v70, 0x78, v176
	v_or_b32_e32 v176, 0x7c, v176
	global_load_dwordx4 v[48:51], v[36:37], off nt
	v_lshl_add_u64 v[36:37], v[78:79], 3, s[10:11]
	v_mov_b32_e32 v75, v177
	v_lshl_add_u64 v[68:69], v[176:177], 3, s[10:11]
	global_load_dword v80, v[36:37], off offset:4
	v_mov_b32_e32 v71, v177
	global_load_dword v68, v[68:69], off offset:4
	v_lshlrev_b64 v[36:37], 12, v[74:75]
	v_lshl_add_u64 v[36:37], v[184:185], 0, v[36:37]
	global_load_dwordx4 v[44:47], v[36:37], off nt
	v_lshl_add_u64 v[36:37], v[74:75], 3, s[10:11]
	global_load_dword v76, v[36:37], off offset:4
	v_lshlrev_b64 v[36:37], 12, v[70:71]
	v_lshl_add_u64 v[36:37], v[184:185], 0, v[36:37]
	global_load_dwordx4 v[40:43], v[36:37], off nt
	v_lshl_add_u64 v[36:37], v[70:71], 3, s[10:11]
	global_load_dword v72, v[36:37], off offset:4
	v_lshlrev_b64 v[36:37], 12, v[176:177]
	v_lshl_add_u64 v[36:37], v[184:185], 0, v[36:37]
	global_load_dwordx4 v[36:39], v[36:37], off nt
	ds_write_b128 v216, v[20:23]
	ds_write_b128 v217, v[24:27]
	ds_write_b128 v218, v[28:31]
	ds_write_b128 v219, v[32:35]
	s_waitcnt lgkmcnt(0)
	ds_read_b128 v[20:23], v220
	s_waitcnt vmcnt(18) lgkmcnt(0)
	v_pk_mul_f32 v[20:21], v[98:99], v[20:21] op_sel_hi:[0,1]
	v_pk_fma_f32 v[20:21], v[178:179], v[20:21], v[64:65]
	v_pk_mul_f32 v[22:23], v[98:99], v[22:23] op_sel_hi:[0,1]
	v_pk_fma_f32 v[22:23], v[180:181], v[22:23], v[66:67]
	v_pk_mul_f32 v[24:25], v[20:21], v[20:21]
	v_pk_mul_f32 v[26:27], v[22:23], v[22:23]
	v_add_f32_e32 v24, v24, v25
	v_add_f32_e32 v24, v26, v24
	v_add_f32_e32 v24, v27, v24
	s_nop 1
	v_mov_b32_dpp v25, v24 row_ror:8 row_mask:0xf bank_mask:0xf
	s_waitcnt lgkmcnt(0)
	v_add_f32_e32 v24, v24, v25
	s_nop 1
	v_mov_b32_dpp v25, v24 row_ror:4 row_mask:0xf bank_mask:0xf
	s_waitcnt lgkmcnt(0)
	v_add_f32_e32 v26, v24, v25
	s_nop 1
	v_mov_b32_dpp v27, v26 quad_perm:[2,3,0,1] row_mask:0xf bank_mask:0xf
	v_cvt_pk_bf16_f32 v24, v20, v21
	v_cvt_pk_bf16_f32 v25, v22, v23
	v_lshlrev_b64 v[22:23], 11, v[96:97]
	v_lshl_add_u64 v[22:23], s[24:25], 0, v[22:23]
	s_waitcnt lgkmcnt(0)
	v_add_f32_e32 v20, v26, v27
	s_nop 1
	v_mov_b32_dpp v21, v20 quad_perm:[1,0,3,2] row_mask:0xf bank_mask:0xf
	v_lshl_add_u64 v[22:23], v[22:23], 0, v[2:3]
	global_store_dwordx2 v[22:23], v[24:25], off
	s_and_saveexec_b64 s[0:1], vcc
	s_cbranch_execz .LBB0_583
	v_lshlrev_b64 v[22:23], 6, v[96:97]
	v_lshl_add_u64 v[22:23], s[6:7], 0, v[22:23]
	v_lshl_add_u64 v[22:23], s[22:23], 2, v[22:23]
	v_mov_b32_e32 v183, v3
	v_lshl_add_u64 v[22:23], v[22:23], 0, v[182:183]
	s_waitcnt lgkmcnt(0)
	v_add_f32_e32 v20, v20, v21
	global_store_dword v[22:23], v20, off
; __device__ __forceinline__ uint2 pack4(f32x4 v) { uint2 r; r.x = pack2(v[0], v[1]); r.y = pack2(v[2], v[3]); return r; }
;     __device__ __forceinline__ void epilogue(f32x4 (&acc)[8][4], const Desc& d, unsigned char* stg) const {
;     ...
;         for (int m = 0; m < 8; ++m) {
;             float4 xc[4]; float fc[4];
; #pragma unroll
;             for (int i2 = 0; i2 < 4; ++i2) { xc[i2] = xn[i2]; fc[i2] = fn[i2]; }
;             if (m < 7) {
; #pragma unroll
;                 for (int i2 = 0; i2 < 4; ++i2) { xn[i2] = *(const float4*)(p.x + (rowb + (m + 1) * 16 + i2 * 4) * D + col); fn[i2] = p.rs[rowb + (m + 1) * 16 + i2 * 4].y; }
;             }
; #pragma unroll
;             for (int n = 0; n < 4; ++n) stgf_put(stg, n, acc[m][n], l15, gq);
;             asm volatile("s_waitcnt lgkmcnt(0)" ::: "memory");
; #pragma unroll
;             for (int i2 = 0; i2 < 4; ++i2) {
;                 const int rl = i2 * 4 + rsub;
;                 const size_t row = rowb + m * 16 + i2 * 4;
;                 const f32x4 v = stgf_get(stg, rl, c);
;                 const float fsm = fc[i2];
;                 const float4 xv = xc[i2];
;                 float4 r;
;                 r.x = xv.x + g1.x * (v[0] * fsm); r.y = xv.y + g1.y * (v[1] * fsm); r.z = xv.z + g1.z * (v[2] * fsm); r.w = xv.w + g1.w * (v[3] * fsm);
;                 *(uint2*)(p.x1 + row * D + col) = pack4((f32x4){r.x, r.y, r.z, r.w});
;                 float ss = r.x * r.x + r.y * r.y + r.z * r.z + r.w * r.w;
;                 ss += __shfl_xor(ss, 8); ss += __shfl_xor(ss, 4); ss += __shfl_xor(ss, 2); ss += __shfl_xor(ss, 1);
;                 if (c == 0) p.st2[row * 16 + nt * 4 + wc] = ss;
;             }
.LBB0_583:
	s_or_b64 exec, exec, s[0:1]
	s_waitcnt lgkmcnt(0)
	ds_read_b128 v[20:23], v221
	s_waitcnt vmcnt(16) lgkmcnt(0)
	v_pk_mul_f32 v[20:21], v[94:95], v[20:21] op_sel_hi:[0,1]
	v_pk_mul_f32 v[22:23], v[94:95], v[22:23] op_sel_hi:[0,1]
	v_pk_fma_f32 v[20:21], v[178:179], v[20:21], v[60:61]
	v_pk_fma_f32 v[22:23], v[180:181], v[22:23], v[62:63]
	v_pk_mul_f32 v[24:25], v[20:21], v[20:21]
	v_pk_mul_f32 v[26:27], v[22:23], v[22:23]
	v_add_f32_e32 v24, v24, v25
	v_add_f32_e32 v24, v26, v24
	v_add_f32_e32 v24, v27, v24
	s_nop 1
	v_mov_b32_dpp v25, v24 row_ror:8 row_mask:0xf bank_mask:0xf
	s_waitcnt lgkmcnt(0)
	v_add_f32_e32 v24, v24, v25
	s_nop 1
	v_mov_b32_dpp v25, v24 row_ror:4 row_mask:0xf bank_mask:0xf
	s_waitcnt lgkmcnt(0)
	v_add_f32_e32 v26, v24, v25
	s_nop 1
	v_mov_b32_dpp v27, v26 quad_perm:[2,3,0,1] row_mask:0xf bank_mask:0xf
	v_cvt_pk_bf16_f32 v24, v20, v21
	v_cvt_pk_bf16_f32 v25, v22, v23
	v_lshlrev_b64 v[22:23], 11, v[92:93]
	v_lshl_add_u64 v[22:23], s[24:25], 0, v[22:23]
	s_waitcnt lgkmcnt(0)
	v_add_f32_e32 v20, v26, v27
	s_nop 1
	v_mov_b32_dpp v21, v20 quad_perm:[1,0,3,2] row_mask:0xf bank_mask:0xf
	v_lshl_add_u64 v[22:23], v[22:23], 0, v[2:3]
	global_store_dwordx2 v[22:23], v[24:25], off
	s_and_saveexec_b64 s[0:1], vcc
	s_cbranch_execz .LBB0_585
	v_lshlrev_b64 v[22:23], 6, v[92:93]
	v_lshl_add_u64 v[22:23], s[6:7], 0, v[22:23]
	v_lshl_add_u64 v[22:23], s[22:23], 2, v[22:23]
	v_mov_b32_e32 v183, v3
	v_lshl_add_u64 v[22:23], v[22:23], 0, v[182:183]
	s_waitcnt lgkmcnt(0)
	v_add_f32_e32 v20, v20, v21
	global_store_dword v[22:23], v20, off
.LBB0_585:
	s_or_b64 exec, exec, s[0:1]
	s_waitcnt lgkmcnt(0)
	ds_read_b128 v[20:23], v159
	s_waitcnt vmcnt(15) lgkmcnt(0)
	v_pk_mul_f32 v[20:21], v[90:91], v[20:21] op_sel_hi:[0,1]
	v_pk_mul_f32 v[22:23], v[90:91], v[22:23] op_sel_hi:[0,1]
	v_pk_fma_f32 v[20:21], v[178:179], v[20:21], v[56:57]
	v_pk_fma_f32 v[22:23], v[180:181], v[22:23], v[58:59]
	v_pk_mul_f32 v[24:25], v[20:21], v[20:21]
	v_pk_mul_f32 v[26:27], v[22:23], v[22:23]
	v_add_f32_e32 v24, v24, v25
	v_add_f32_e32 v24, v26, v24
	v_add_f32_e32 v24, v27, v24
	s_nop 1
	v_mov_b32_dpp v25, v24 row_ror:8 row_mask:0xf bank_mask:0xf
	s_waitcnt lgkmcnt(0)
	v_add_f32_e32 v24, v24, v25
	s_nop 1
	v_mov_b32_dpp v25, v24 row_ror:4 row_mask:0xf bank_mask:0xf
	s_waitcnt lgkmcnt(0)
	v_add_f32_e32 v26, v24, v25
	s_nop 1
	v_mov_b32_dpp v27, v26 quad_perm:[2,3,0,1] row_mask:0xf bank_mask:0xf
	v_cvt_pk_bf16_f32 v24, v20, v21
	v_cvt_pk_bf16_f32 v25, v22, v23
	v_lshlrev_b64 v[22:23], 11, v[88:89]
	v_lshl_add_u64 v[22:23], s[24:25], 0, v[22:23]
	s_waitcnt lgkmcnt(0)
	v_add_f32_e32 v20, v26, v27
	s_nop 1
	v_mov_b32_dpp v21, v20 quad_perm:[1,0,3,2] row_mask:0xf bank_mask:0xf
	v_lshl_add_u64 v[22:23], v[22:23], 0, v[2:3]
	global_store_dwordx2 v[22:23], v[24:25], off
	s_and_saveexec_b64 s[0:1], vcc
	s_cbranch_execz .LBB0_587
	v_lshlrev_b64 v[22:23], 6, v[88:89]
	v_lshl_add_u64 v[22:23], s[6:7], 0, v[22:23]
	v_lshl_add_u64 v[22:23], s[22:23], 2, v[22:23]
	v_mov_b32_e32 v183, v3
	v_lshl_add_u64 v[22:23], v[22:23], 0, v[182:183]
	s_waitcnt lgkmcnt(0)
	v_add_f32_e32 v20, v20, v21
	global_store_dword v[22:23], v20, off
.LBB0_587:
	s_or_b64 exec, exec, s[0:1]
	s_waitcnt lgkmcnt(0)
	ds_read_b128 v[20:23], v151
	s_waitcnt lgkmcnt(0)
	v_pk_mul_f32 v[20:21], v[86:87], v[20:21] op_sel_hi:[0,1]
	v_pk_mul_f32 v[22:23], v[86:87], v[22:23] op_sel_hi:[0,1]
	s_waitcnt vmcnt(15)
	v_pk_fma_f32 v[20:21], v[178:179], v[20:21], v[52:53]
	v_pk_fma_f32 v[22:23], v[180:181], v[22:23], v[54:55]
	v_pk_mul_f32 v[24:25], v[20:21], v[20:21]
	v_pk_mul_f32 v[26:27], v[22:23], v[22:23]
	v_add_f32_e32 v24, v24, v25
	v_add_f32_e32 v24, v26, v24
	v_add_f32_e32 v24, v27, v24
	s_nop 1
	v_mov_b32_dpp v25, v24 row_ror:8 row_mask:0xf bank_mask:0xf
	s_waitcnt lgkmcnt(0)
	v_add_f32_e32 v24, v24, v25
	s_nop 1
	v_mov_b32_dpp v25, v24 row_ror:4 row_mask:0xf bank_mask:0xf
	s_waitcnt lgkmcnt(0)
	v_add_f32_e32 v26, v24, v25
	s_nop 1
	v_mov_b32_dpp v27, v26 quad_perm:[2,3,0,1] row_mask:0xf bank_mask:0xf
	v_cvt_pk_bf16_f32 v24, v20, v21
	v_cvt_pk_bf16_f32 v25, v22, v23
	v_lshlrev_b64 v[22:23], 11, v[84:85]
	v_lshl_add_u64 v[22:23], s[24:25], 0, v[22:23]
	s_waitcnt lgkmcnt(0)
	v_add_f32_e32 v20, v26, v27
	s_nop 1
	v_mov_b32_dpp v21, v20 quad_perm:[1,0,3,2] row_mask:0xf bank_mask:0xf
	v_lshl_add_u64 v[22:23], v[22:23], 0, v[2:3]
	global_store_dwordx2 v[22:23], v[24:25], off
	s_and_saveexec_b64 s[0:1], vcc
	s_cbranch_execz .LBB0_589
	v_lshlrev_b64 v[22:23], 6, v[84:85]
	v_lshl_add_u64 v[22:23], s[6:7], 0, v[22:23]
	v_lshl_add_u64 v[22:23], s[22:23], 2, v[22:23]
	v_mov_b32_e32 v183, v3
	v_lshl_add_u64 v[22:23], v[22:23], 0, v[182:183]
	s_waitcnt lgkmcnt(0)
	v_add_f32_e32 v20, v20, v21
	global_store_dword v[22:23], v20, off
; __device__ __forceinline__ uint2 pack4(f32x4 v) { uint2 r; r.x = pack2(v[0], v[1]); r.y = pack2(v[2], v[3]); return r; }
;     __device__ __forceinline__ void epilogue(f32x4 (&acc)[8][4], const Desc& d, unsigned char* stg) const {
;     ...
;         for (int m = 0; m < 8; ++m) {
;             float4 xc[4]; float fc[4];
; #pragma unroll
;             for (int i2 = 0; i2 < 4; ++i2) { xc[i2] = xn[i2]; fc[i2] = fn[i2]; }
;             if (m < 7) {
; #pragma unroll
;                 for (int i2 = 0; i2 < 4; ++i2) { xn[i2] = *(const float4*)(p.x + (rowb + (m + 1) * 16 + i2 * 4) * D + col); fn[i2] = p.rs[rowb + (m + 1) * 16 + i2 * 4].y; }
;             }
; #pragma unroll
;             for (int n = 0; n < 4; ++n) stgf_put(stg, n, acc[m][n], l15, gq);
;             asm volatile("s_waitcnt lgkmcnt(0)" ::: "memory");
; #pragma unroll
;             for (int i2 = 0; i2 < 4; ++i2) {
;                 const int rl = i2 * 4 + rsub;
;                 const size_t row = rowb + m * 16 + i2 * 4;
;                 const f32x4 v = stgf_get(stg, rl, c);
;                 const float fsm = fc[i2];
;                 const float4 xv = xc[i2];
;                 float4 r;
;                 r.x = xv.x + g1.x * (v[0] * fsm); r.y = xv.y + g1.y * (v[1] * fsm); r.z = xv.z + g1.z * (v[2] * fsm); r.w = xv.w + g1.w * (v[3] * fsm);
;                 *(uint2*)(p.x1 + row * D + col) = pack4((f32x4){r.x, r.y, r.z, r.w});
;                 float ss = r.x * r.x + r.y * r.y + r.z * r.z + r.w * r.w;
;                 ss += __shfl_xor(ss, 8); ss += __shfl_xor(ss, 4); ss += __shfl_xor(ss, 2); ss += __shfl_xor(ss, 1);
;                 if (c == 0) p.st2[row * 16 + nt * 4 + wc] = ss;
;             }
.LBB0_589:
	s_or_b64 exec, exec, s[0:1]
	s_waitcnt lgkmcnt(0)
	ds_write_b128 v216, v[4:7]
	ds_write_b128 v217, v[8:11]
	ds_write_b128 v218, v[12:15]
	ds_write_b128 v219, v[16:19]
	s_waitcnt lgkmcnt(0)
	ds_read_b128 v[4:7], v220
	s_waitcnt vmcnt(10) lgkmcnt(0)
	v_pk_mul_f32 v[4:5], v[80:81], v[4:5] op_sel_hi:[0,1]
	v_pk_fma_f32 v[4:5], v[178:179], v[4:5], v[48:49]
	v_pk_mul_f32 v[6:7], v[80:81], v[6:7] op_sel_hi:[0,1]
	v_pk_fma_f32 v[6:7], v[180:181], v[6:7], v[50:51]
	v_pk_mul_f32 v[8:9], v[4:5], v[4:5]
	v_pk_mul_f32 v[10:11], v[6:7], v[6:7]
	v_add_f32_e32 v8, v8, v9
	v_add_f32_e32 v8, v10, v8
	v_add_f32_e32 v8, v11, v8
	s_nop 1
	v_mov_b32_dpp v9, v8 row_ror:8 row_mask:0xf bank_mask:0xf
	s_waitcnt lgkmcnt(0)
	v_add_f32_e32 v8, v8, v9
	s_nop 1
	v_mov_b32_dpp v9, v8 row_ror:4 row_mask:0xf bank_mask:0xf
	s_waitcnt lgkmcnt(0)
	v_add_f32_e32 v10, v8, v9
	s_nop 1
	v_mov_b32_dpp v11, v10 quad_perm:[2,3,0,1] row_mask:0xf bank_mask:0xf
	v_cvt_pk_bf16_f32 v8, v4, v5
	v_cvt_pk_bf16_f32 v9, v6, v7
	v_lshlrev_b64 v[6:7], 11, v[78:79]
	v_lshl_add_u64 v[6:7], s[24:25], 0, v[6:7]
	s_waitcnt lgkmcnt(0)
	v_add_f32_e32 v4, v10, v11
	s_nop 1
	v_mov_b32_dpp v5, v4 quad_perm:[1,0,3,2] row_mask:0xf bank_mask:0xf
	v_lshl_add_u64 v[6:7], v[6:7], 0, v[2:3]
	global_store_dwordx2 v[6:7], v[8:9], off
	s_and_saveexec_b64 s[0:1], vcc
	s_cbranch_execz .LBB0_591
	v_lshlrev_b64 v[6:7], 6, v[78:79]
	v_lshl_add_u64 v[6:7], s[6:7], 0, v[6:7]
	v_lshl_add_u64 v[6:7], s[22:23], 2, v[6:7]
	v_mov_b32_e32 v183, v3
	v_lshl_add_u64 v[6:7], v[6:7], 0, v[182:183]
	s_waitcnt lgkmcnt(0)
	v_add_f32_e32 v4, v4, v5
	global_store_dword v[6:7], v4, off
.LBB0_591:
	s_or_b64 exec, exec, s[0:1]
	s_waitcnt lgkmcnt(0)
	ds_read_b128 v[4:7], v221
	s_waitcnt vmcnt(8) lgkmcnt(0)
	v_pk_mul_f32 v[4:5], v[76:77], v[4:5] op_sel_hi:[0,1]
	v_pk_mul_f32 v[6:7], v[76:77], v[6:7] op_sel_hi:[0,1]
	v_pk_fma_f32 v[4:5], v[178:179], v[4:5], v[44:45]
	v_pk_fma_f32 v[6:7], v[180:181], v[6:7], v[46:47]
	v_pk_mul_f32 v[8:9], v[4:5], v[4:5]
	v_pk_mul_f32 v[10:11], v[6:7], v[6:7]
	v_add_f32_e32 v8, v8, v9
	v_add_f32_e32 v8, v10, v8
	v_add_f32_e32 v8, v11, v8
	s_nop 1
	v_mov_b32_dpp v9, v8 row_ror:8 row_mask:0xf bank_mask:0xf
	s_waitcnt lgkmcnt(0)
	v_add_f32_e32 v8, v8, v9
	s_nop 1
	v_mov_b32_dpp v9, v8 row_ror:4 row_mask:0xf bank_mask:0xf
	s_waitcnt lgkmcnt(0)
	v_add_f32_e32 v10, v8, v9
	s_nop 1
	v_mov_b32_dpp v11, v10 quad_perm:[2,3,0,1] row_mask:0xf bank_mask:0xf
	v_cvt_pk_bf16_f32 v8, v4, v5
	v_cvt_pk_bf16_f32 v9, v6, v7
	v_lshlrev_b64 v[6:7], 11, v[74:75]
	v_lshl_add_u64 v[6:7], s[24:25], 0, v[6:7]
	s_waitcnt lgkmcnt(0)
	v_add_f32_e32 v4, v10, v11
	s_nop 1
	v_mov_b32_dpp v5, v4 quad_perm:[1,0,3,2] row_mask:0xf bank_mask:0xf
	v_lshl_add_u64 v[6:7], v[6:7], 0, v[2:3]
	global_store_dwordx2 v[6:7], v[8:9], off
	s_and_saveexec_b64 s[0:1], vcc
	s_cbranch_execz .LBB0_593
	v_lshlrev_b64 v[6:7], 6, v[74:75]
	v_lshl_add_u64 v[6:7], s[6:7], 0, v[6:7]
	v_lshl_add_u64 v[6:7], s[22:23], 2, v[6:7]
	v_mov_b32_e32 v183, v3
	v_lshl_add_u64 v[6:7], v[6:7], 0, v[182:183]
	s_waitcnt lgkmcnt(0)
	v_add_f32_e32 v4, v4, v5
	global_store_dword v[6:7], v4, off
.LBB0_593:
	s_or_b64 exec, exec, s[0:1]
	s_waitcnt lgkmcnt(0)
	ds_read_b128 v[4:7], v159
	s_waitcnt vmcnt(7) lgkmcnt(0)
	v_pk_mul_f32 v[4:5], v[72:73], v[4:5] op_sel_hi:[0,1]
	v_pk_mul_f32 v[6:7], v[72:73], v[6:7] op_sel_hi:[0,1]
	v_pk_fma_f32 v[4:5], v[178:179], v[4:5], v[40:41]
	v_pk_fma_f32 v[6:7], v[180:181], v[6:7], v[42:43]
	v_pk_mul_f32 v[8:9], v[4:5], v[4:5]
	v_pk_mul_f32 v[10:11], v[6:7], v[6:7]
	v_add_f32_e32 v8, v8, v9
	v_add_f32_e32 v8, v10, v8
	v_add_f32_e32 v8, v11, v8
	s_nop 1
	v_mov_b32_dpp v9, v8 row_ror:8 row_mask:0xf bank_mask:0xf
	s_waitcnt lgkmcnt(0)
	v_add_f32_e32 v8, v8, v9
	s_nop 1
	v_mov_b32_dpp v9, v8 row_ror:4 row_mask:0xf bank_mask:0xf
	s_waitcnt lgkmcnt(0)
	v_add_f32_e32 v10, v8, v9
	s_nop 1
	v_mov_b32_dpp v11, v10 quad_perm:[2,3,0,1] row_mask:0xf bank_mask:0xf
	v_cvt_pk_bf16_f32 v8, v4, v5
	v_cvt_pk_bf16_f32 v9, v6, v7
	v_lshlrev_b64 v[6:7], 11, v[70:71]
	v_lshl_add_u64 v[6:7], s[24:25], 0, v[6:7]
	s_waitcnt lgkmcnt(0)
	v_add_f32_e32 v4, v10, v11
	s_nop 1
	v_mov_b32_dpp v5, v4 quad_perm:[1,0,3,2] row_mask:0xf bank_mask:0xf
	v_lshl_add_u64 v[6:7], v[6:7], 0, v[2:3]
	global_store_dwordx2 v[6:7], v[8:9], off
	s_and_saveexec_b64 s[0:1], vcc
	s_cbranch_execz .LBB0_595
	v_lshlrev_b64 v[6:7], 6, v[70:71]
	v_lshl_add_u64 v[6:7], s[6:7], 0, v[6:7]
	v_lshl_add_u64 v[6:7], s[22:23], 2, v[6:7]
	v_mov_b32_e32 v183, v3
	v_lshl_add_u64 v[6:7], v[6:7], 0, v[182:183]
	s_waitcnt lgkmcnt(0)
	v_add_f32_e32 v4, v4, v5
	global_store_dword v[6:7], v4, off
.LBB0_595:
	s_or_b64 exec, exec, s[0:1]
	s_waitcnt lgkmcnt(0)
	ds_read_b128 v[4:7], v151
	s_waitcnt lgkmcnt(0)
	v_pk_mul_f32 v[4:5], v[68:69], v[4:5] op_sel_hi:[0,1]
	v_pk_mul_f32 v[6:7], v[68:69], v[6:7] op_sel_hi:[0,1]
	s_waitcnt vmcnt(7)
	v_pk_fma_f32 v[4:5], v[178:179], v[4:5], v[36:37]
	v_pk_fma_f32 v[6:7], v[180:181], v[6:7], v[38:39]
	v_pk_mul_f32 v[8:9], v[4:5], v[4:5]
	v_pk_mul_f32 v[10:11], v[6:7], v[6:7]
	v_add_f32_e32 v8, v8, v9
	v_add_f32_e32 v8, v10, v8
	v_add_f32_e32 v8, v11, v8
	s_nop 1
	v_mov_b32_dpp v9, v8 row_ror:8 row_mask:0xf bank_mask:0xf
	s_waitcnt lgkmcnt(0)
	v_add_f32_e32 v8, v8, v9
	s_nop 1
	v_mov_b32_dpp v9, v8 row_ror:4 row_mask:0xf bank_mask:0xf
	s_waitcnt lgkmcnt(0)
	v_add_f32_e32 v10, v8, v9
	s_nop 1
	v_mov_b32_dpp v11, v10 quad_perm:[2,3,0,1] row_mask:0xf bank_mask:0xf
	v_cvt_pk_bf16_f32 v8, v4, v5
	v_cvt_pk_bf16_f32 v9, v6, v7
	v_lshlrev_b64 v[6:7], 11, v[176:177]
	v_lshl_add_u64 v[6:7], s[24:25], 0, v[6:7]
	s_waitcnt lgkmcnt(0)
	v_add_f32_e32 v4, v10, v11
	s_nop 1
	v_mov_b32_dpp v5, v4 quad_perm:[1,0,3,2] row_mask:0xf bank_mask:0xf
	v_lshl_add_u64 v[6:7], v[6:7], 0, v[2:3]
	global_store_dwordx2 v[6:7], v[8:9], off
	s_and_saveexec_b64 s[0:1], vcc
	s_cbranch_execz .LBB0_499
	v_lshlrev_b64 v[6:7], 6, v[176:177]
	v_lshl_add_u64 v[6:7], s[6:7], 0, v[6:7]
	v_lshl_add_u64 v[6:7], s[22:23], 2, v[6:7]
	v_mov_b32_e32 v183, v3
	v_lshl_add_u64 v[6:7], v[6:7], 0, v[182:183]
	s_waitcnt lgkmcnt(0)
	v_add_f32_e32 v2, v4, v5
	global_store_dword v[6:7], v2, off
	s_branch .LBB0_499
